# GELU epilogue bias quads requested at unit start (registers unused by the K loop) instead of at the epilogue start
# baseline (speedup 1.0000x reference)
.LBB0_1768:
	s_ashr_i32 s53, s52, 31
	s_lshl_b64 s[60:61], s[52:53], 19
	s_add_u32 s5, s90, s60
	s_addc_u32 s51, s91, s61
	s_and_b64 s[60:61], s[64:65], exec
	s_cselect_b32 s60, s5, s6
	s_cselect_b32 s61, s51, s7
	s_ashr_i32 s51, s50, 31
	s_lshl_b64 s[72:73], s[50:51], 19
	s_add_u32 s5, s3, s72
	s_addc_u32 s51, s21, s73
	s_and_b64 s[64:65], s[64:65], exec
	s_cselect_b32 s64, s5, s70
	s_cselect_b32 s65, s51, s71
	s_add_u32 s5, s70, 0x100
	s_addc_u32 s51, s71, 0
	s_add_u32 s6, s6, 0x60080
	v_mov_b32_e32 v0, 0
	s_addc_u32 s7, s7, 0
	s_mov_b32 s53, -2
	v_mov_b64_e32 v[0:1], 0
	v_mov_b64_e32 v[2:3], 0
	v_mov_b64_e32 v[4:5], 0
	v_mov_b64_e32 v[6:7], 0
	v_mov_b64_e32 v[16:17], 0
	v_mov_b64_e32 v[18:19], 0
	v_mov_b64_e32 v[20:21], 0
	v_mov_b64_e32 v[22:23], 0
	s_waitcnt vmcnt(0)
	v_mbcnt_lo_u32_b32 v220, -1, 0
	v_mbcnt_hi_u32_b32 v220, -1, v220
	v_readlane_b32 s100, v249, 28
	v_readlane_b32 s101, v249, 29
	v_bfe_u32 v220, v220, 4, 2
	v_mov_b32_e32 v221, s4
	v_lshlrev_b32_e32 v220, 3, v220
	v_lshl_or_b32 v220, v221, 8, v220
	v_or_b32_e32 v220, s41, v220
	v_lshlrev_b32_e32 v220, 2, v220
	global_load_dwordx4 v[204:207], v220, s[100:101]
	global_load_dwordx4 v[208:211], v220, s[100:101] offset:16
	global_load_dwordx4 v[212:215], v220, s[100:101] offset:512
	global_load_dwordx4 v[216:219], v220, s[100:101] offset:528
	v_mov_b64_e32 v[32:33], 0
	v_mov_b64_e32 v[34:35], 0
	v_mov_b64_e32 v[36:37], 0
	v_mov_b64_e32 v[38:39], 0
	v_mov_b64_e32 v[48:49], 0
	v_mov_b64_e32 v[50:51], 0
	v_mov_b64_e32 v[52:53], 0
	v_mov_b64_e32 v[54:55], 0
	v_mov_b64_e32 v[8:9], 0
	v_mov_b64_e32 v[10:11], 0
	v_mov_b64_e32 v[12:13], 0
	v_mov_b64_e32 v[14:15], 0
	v_mov_b64_e32 v[24:25], 0
	v_mov_b64_e32 v[26:27], 0
	v_mov_b64_e32 v[28:29], 0
	v_mov_b64_e32 v[30:31], 0
	v_mov_b64_e32 v[40:41], 0
	v_mov_b64_e32 v[42:43], 0
	v_mov_b64_e32 v[44:45], 0
	v_mov_b64_e32 v[46:47], 0
	v_mov_b64_e32 v[64:65], 0
	v_mov_b64_e32 v[66:67], 0
	v_mov_b64_e32 v[72:73], 0
	v_mov_b64_e32 v[74:75], 0
	v_mov_b64_e32 v[80:81], 0
	v_mov_b64_e32 v[82:83], 0
	v_mov_b64_e32 v[84:85], 0
	v_mov_b64_e32 v[86:87], 0
	v_mov_b64_e32 v[96:97], 0
	v_mov_b64_e32 v[98:99], 0
	v_mov_b64_e32 v[100:101], 0
	v_mov_b64_e32 v[102:103], 0
	v_mov_b64_e32 v[112:113], 0
	v_mov_b64_e32 v[114:115], 0
	v_mov_b64_e32 v[116:117], 0
	v_mov_b64_e32 v[118:119], 0
	v_mov_b64_e32 v[128:129], 0
	v_mov_b64_e32 v[130:131], 0
	v_mov_b64_e32 v[132:133], 0
	v_mov_b64_e32 v[134:135], 0
	v_mov_b64_e32 v[88:89], 0
	v_mov_b64_e32 v[90:91], 0
	v_mov_b64_e32 v[92:93], 0
	v_mov_b64_e32 v[94:95], 0
	v_mov_b64_e32 v[104:105], 0
	v_mov_b64_e32 v[106:107], 0
	v_mov_b64_e32 v[108:109], 0
	v_mov_b64_e32 v[110:111], 0
	v_mov_b64_e32 v[120:121], 0
	v_mov_b64_e32 v[122:123], 0
	v_mov_b64_e32 v[124:125], 0
	v_mov_b64_e32 v[126:127], 0
	v_mov_b64_e32 v[136:137], 0
	v_mov_b64_e32 v[138:139], 0
	v_mov_b64_e32 v[140:141], 0
	v_mov_b64_e32 v[142:143], 0

.LBB0_1772:
	s_mov_b32 s5, 0
	v_mbcnt_lo_u32_b32 v147, -1, 0
	v_mbcnt_hi_u32_b32 v147, -1, v147
	s_lshl_b32 s5, s4, 8
	v_readlane_b32 s80, v249, 18
	v_bfe_u32 v58, v147, 4, 2
	v_lshlrev_b32_e32 v146, 3, v58
	v_or_b32_e32 v56, s41, v146
	v_or_b32_e32 v56, s5, v56
	v_ashrrev_i32_e32 v57, 31, v56
	v_readlane_b32 s90, v249, 28
	v_readlane_b32 s91, v249, 29
	v_cmp_eq_u32_e64 s[6:7], 0, v58
	s_add_i32 s51, s5, 0xfffff800
	v_lshl_add_u64 v[60:61], v[56:57], 2, s[90:91]
	s_nop 0
	s_cmp_gt_i32 s4, 7
	v_readlane_b32 s81, v249, 19
	v_readlane_b32 s82, v249, 20
	v_readlane_b32 s83, v249, 21
	v_readlane_b32 s84, v249, 22
	v_readlane_b32 s85, v249, 23
	v_readlane_b32 s86, v249, 24
	v_readlane_b32 s87, v249, 25
	s_cselect_b64 s[70:71], -1, 0
	s_and_b64 s[72:73], s[70:71], exec
	s_mov_b32 s53, 0x16500000
	v_readlane_b32 s80, v249, 55
	s_cselect_b32 s53, s53, 0x12500000
	v_readlane_b32 s86, v249, 61
	s_cselect_b32 s5, s51, s5
	v_readlane_b32 s87, v249, 62
	s_add_u32 s72, s86, s53
	s_addc_u32 s73, s87, 0
	s_lshl_b32 s51, s68, 8
	s_or_b32 s5, s41, s5
	s_add_i32 s51, s51, s39
	v_or_b32_e32 v146, s5, v146
	v_and_or_b32 v148, v147, 15, s51
	v_ashrrev_i32_e32 v147, 31, v146
	v_ashrrev_i32_e32 v149, 31, v148
	v_lshl_add_u64 v[146:147], v[146:147], 1, s[72:73]
	v_lshlrev_b64 v[160:161], 12, v[148:149]
	v_lshl_add_u64 v[164:165], v[146:147], 0, v[160:161]
	v_mov_b64_e32 v[150:151], s[24:25]
	s_lshl_b32 s53, s4, 2
	s_sub_i32 s68, s53, 32
	s_ashr_i32 s69, s68, 31
	s_or_b64 s[68:69], s[68:69], s[14:15]
	s_cmp_lt_i32 s4, 8
	v_readlane_b32 s88, v249, 26
	v_readlane_b32 s89, v249, 27
	v_readlane_b32 s92, v249, 30
	v_readlane_b32 s93, v249, 31
	v_readlane_b32 s94, v249, 32
	v_readlane_b32 s95, v249, 33
	v_readlane_b32 s81, v249, 56
	v_readlane_b32 s82, v249, 57
	v_readlane_b32 s83, v249, 58
	v_readlane_b32 s84, v249, 59
	v_readlane_b32 s85, v249, 60
	s_waitcnt vmcnt(0)
	v_readlane_b32 s90, v249, 63
	v_readlane_b32 s91, v248, 0
	s_mov_b64 s[94:95], s[46:47]
	v_mov_b32_e32 v192, v148
	v_ashrrev_i32_e32 v193, 31, v192
	v_lshlrev_b64 v[194:195], 12, v[192:193]
	v_lshl_add_u64 v[196:197], v[146:147], 0, v[194:195]
	v_pk_add_f32 v[140:141], v[140:141], v[204:205]
	v_pk_add_f32 v[142:143], v[142:143], v[206:207]
	v_pk_add_f32 v[136:137], v[136:137], v[208:209]
	v_pk_add_f32 v[138:139], v[138:139], v[210:211]
	v_med3_f32 v160, v140, s78, v158
	v_med3_f32 v161, v141, s78, v158
	v_med3_f32 v162, v142, s78, v158
	v_med3_f32 v163, v143, s78, v158
	v_med3_f32 v164, v136, s78, v158
	v_med3_f32 v165, v137, s78, v158
	v_med3_f32 v166, v138, s78, v158
	v_med3_f32 v167, v139, s78, v158
	v_pk_mul_f32 v[168:169], v[160:161], v[160:161]
	v_pk_mul_f32 v[170:171], v[162:163], v[162:163]
	v_pk_mul_f32 v[172:173], v[164:165], v[164:165]
	v_pk_mul_f32 v[174:175], v[166:167], v[166:167]
	v_pk_fma_f32 v[168:169], v[168:169], s[20:21], -1.0 op_sel_hi:[1,0,0]
	v_pk_fma_f32 v[170:171], v[170:171], s[20:21], -1.0 op_sel_hi:[1,0,0]
	v_pk_fma_f32 v[172:173], v[172:173], s[20:21], -1.0 op_sel_hi:[1,0,0]
	v_pk_fma_f32 v[174:175], v[174:175], s[20:21], -1.0 op_sel_hi:[1,0,0]
	v_pk_fma_f32 v[176:177], v[168:169], s[22:23], v[150:151] op_sel_hi:[1,0,0] neg_lo:[1,0,0] neg_hi:[1,0,0]
	v_pk_fma_f32 v[178:179], v[170:171], s[22:23], v[150:151] op_sel_hi:[1,0,0] neg_lo:[1,0,0] neg_hi:[1,0,0]
	v_pk_fma_f32 v[180:181], v[172:173], s[22:23], v[150:151] op_sel_hi:[1,0,0] neg_lo:[1,0,0] neg_hi:[1,0,0]
	v_pk_fma_f32 v[182:183], v[174:175], s[22:23], v[150:151] op_sel_hi:[1,0,0] neg_lo:[1,0,0] neg_hi:[1,0,0]
	v_pk_fma_f32 v[176:177], v[168:169], v[176:177], s[26:27] op_sel_hi:[1,1,0]
	v_pk_fma_f32 v[178:179], v[170:171], v[178:179], s[26:27] op_sel_hi:[1,1,0]
	v_pk_fma_f32 v[180:181], v[172:173], v[180:181], s[26:27] op_sel_hi:[1,1,0]
	v_pk_fma_f32 v[182:183], v[174:175], v[182:183], s[26:27] op_sel_hi:[1,1,0]
	v_pk_fma_f32 v[176:177], v[168:169], v[176:177], s[28:29] op_sel_hi:[1,1,0]
	v_pk_fma_f32 v[178:179], v[170:171], v[178:179], s[28:29] op_sel_hi:[1,1,0]
	v_pk_fma_f32 v[180:181], v[172:173], v[180:181], s[28:29] op_sel_hi:[1,1,0]
	v_pk_fma_f32 v[182:183], v[174:175], v[182:183], s[28:29] op_sel_hi:[1,1,0]
	v_pk_fma_f32 v[176:177], v[168:169], v[176:177], s[30:31] op_sel_hi:[1,1,0]
	v_pk_fma_f32 v[178:179], v[170:171], v[178:179], s[30:31] op_sel_hi:[1,1,0]
	v_pk_fma_f32 v[180:181], v[172:173], v[180:181], s[30:31] op_sel_hi:[1,1,0]
	v_pk_fma_f32 v[182:183], v[174:175], v[182:183], s[30:31] op_sel_hi:[1,1,0]
	v_pk_fma_f32 v[176:177], v[168:169], v[176:177], s[34:35] op_sel_hi:[1,1,0]
	v_pk_fma_f32 v[178:179], v[170:171], v[178:179], s[34:35] op_sel_hi:[1,1,0]
	v_pk_fma_f32 v[180:181], v[172:173], v[180:181], s[34:35] op_sel_hi:[1,1,0]
	v_pk_fma_f32 v[182:183], v[174:175], v[182:183], s[34:35] op_sel_hi:[1,1,0]
	v_pk_fma_f32 v[176:177], v[168:169], v[176:177], s[36:37] op_sel_hi:[1,1,0]
	v_pk_fma_f32 v[178:179], v[170:171], v[178:179], s[36:37] op_sel_hi:[1,1,0]
	v_pk_fma_f32 v[180:181], v[172:173], v[180:181], s[36:37] op_sel_hi:[1,1,0]
	v_pk_fma_f32 v[182:183], v[174:175], v[182:183], s[36:37] op_sel_hi:[1,1,0]
	v_pk_fma_f32 v[176:177], v[168:169], v[176:177], s[38:39] op_sel_hi:[1,1,0]
	v_pk_fma_f32 v[178:179], v[170:171], v[178:179], s[38:39] op_sel_hi:[1,1,0]
	v_pk_fma_f32 v[180:181], v[172:173], v[180:181], s[38:39] op_sel_hi:[1,1,0]
	v_pk_fma_f32 v[182:183], v[174:175], v[182:183], s[38:39] op_sel_hi:[1,1,0]
	v_pk_fma_f32 v[176:177], v[168:169], v[176:177], s[40:41] op_sel_hi:[1,1,0]
	v_pk_fma_f32 v[178:179], v[170:171], v[178:179], s[40:41] op_sel_hi:[1,1,0]
	v_pk_fma_f32 v[180:181], v[172:173], v[180:181], s[40:41] op_sel_hi:[1,1,0]
	v_pk_fma_f32 v[182:183], v[174:175], v[182:183], s[40:41] op_sel_hi:[1,1,0]
	v_pk_fma_f32 v[176:177], v[168:169], v[176:177], s[42:43] op_sel_hi:[1,1,0]
	v_pk_fma_f32 v[178:179], v[170:171], v[178:179], s[42:43] op_sel_hi:[1,1,0]
	v_pk_fma_f32 v[180:181], v[172:173], v[180:181], s[42:43] op_sel_hi:[1,1,0]
	v_pk_fma_f32 v[182:183], v[174:175], v[182:183], s[42:43] op_sel_hi:[1,1,0]
	v_pk_fma_f32 v[176:177], v[168:169], v[176:177], s[44:45] op_sel_hi:[1,1,0]
	v_pk_fma_f32 v[178:179], v[170:171], v[178:179], s[44:45] op_sel_hi:[1,1,0]
	v_pk_fma_f32 v[180:181], v[172:173], v[180:181], s[44:45] op_sel_hi:[1,1,0]
	v_pk_fma_f32 v[182:183], v[174:175], v[182:183], s[44:45] op_sel_hi:[1,1,0]
	v_pk_fma_f32 v[168:169], v[168:169], v[176:177], s[48:49] op_sel_hi:[1,1,0]
	v_pk_fma_f32 v[170:171], v[170:171], v[178:179], s[48:49] op_sel_hi:[1,1,0]
	v_pk_fma_f32 v[172:173], v[172:173], v[180:181], s[48:49] op_sel_hi:[1,1,0]
	v_pk_fma_f32 v[174:175], v[174:175], v[182:183], s[48:49] op_sel_hi:[1,1,0]
	v_pk_fma_f32 v[160:161], v[160:161], v[168:169], 0.5 op_sel_hi:[1,1,0]
	v_pk_fma_f32 v[162:163], v[162:163], v[170:171], 0.5 op_sel_hi:[1,1,0]
	v_pk_fma_f32 v[164:165], v[164:165], v[172:173], 0.5 op_sel_hi:[1,1,0]
	v_pk_fma_f32 v[166:167], v[166:167], v[174:175], 0.5 op_sel_hi:[1,1,0]
	v_pk_mul_f32 v[140:141], v[140:141], v[160:161]
	v_pk_mul_f32 v[142:143], v[142:143], v[162:163]
	v_pk_mul_f32 v[136:137], v[136:137], v[164:165]
	v_pk_mul_f32 v[138:139], v[138:139], v[166:167]
	v_cvt_pk_bf16_f32 v184, v140, v141
	v_cvt_pk_bf16_f32 v185, v142, v143
	v_cvt_pk_bf16_f32 v186, v136, v137
	v_cvt_pk_bf16_f32 v187, v138, v139
	global_store_dwordx4 v[196:197], v[184:187], off
	v_pk_add_f32 v[132:133], v[132:133], v[212:213]
	v_pk_add_f32 v[134:135], v[134:135], v[214:215]
	v_pk_add_f32 v[128:129], v[128:129], v[216:217]
	v_pk_add_f32 v[130:131], v[130:131], v[218:219]
	v_med3_f32 v160, v132, s78, v158
	v_med3_f32 v161, v133, s78, v158
	v_med3_f32 v162, v134, s78, v158
	v_med3_f32 v163, v135, s78, v158
	v_med3_f32 v164, v128, s78, v158
	v_med3_f32 v165, v129, s78, v158
	v_med3_f32 v166, v130, s78, v158
	v_med3_f32 v167, v131, s78, v158
	v_pk_mul_f32 v[168:169], v[160:161], v[160:161]
	v_pk_mul_f32 v[170:171], v[162:163], v[162:163]
	v_pk_mul_f32 v[172:173], v[164:165], v[164:165]
	v_pk_mul_f32 v[174:175], v[166:167], v[166:167]
	v_pk_fma_f32 v[168:169], v[168:169], s[20:21], -1.0 op_sel_hi:[1,0,0]
	v_pk_fma_f32 v[170:171], v[170:171], s[20:21], -1.0 op_sel_hi:[1,0,0]
	v_pk_fma_f32 v[172:173], v[172:173], s[20:21], -1.0 op_sel_hi:[1,0,0]
	v_pk_fma_f32 v[174:175], v[174:175], s[20:21], -1.0 op_sel_hi:[1,0,0]
	v_pk_fma_f32 v[176:177], v[168:169], s[22:23], v[150:151] op_sel_hi:[1,0,0] neg_lo:[1,0,0] neg_hi:[1,0,0]
	v_pk_fma_f32 v[178:179], v[170:171], s[22:23], v[150:151] op_sel_hi:[1,0,0] neg_lo:[1,0,0] neg_hi:[1,0,0]
	v_pk_fma_f32 v[180:181], v[172:173], s[22:23], v[150:151] op_sel_hi:[1,0,0] neg_lo:[1,0,0] neg_hi:[1,0,0]
	v_pk_fma_f32 v[182:183], v[174:175], s[22:23], v[150:151] op_sel_hi:[1,0,0] neg_lo:[1,0,0] neg_hi:[1,0,0]
	v_pk_fma_f32 v[176:177], v[168:169], v[176:177], s[26:27] op_sel_hi:[1,1,0]
	v_pk_fma_f32 v[178:179], v[170:171], v[178:179], s[26:27] op_sel_hi:[1,1,0]
	v_pk_fma_f32 v[180:181], v[172:173], v[180:181], s[26:27] op_sel_hi:[1,1,0]
	v_pk_fma_f32 v[182:183], v[174:175], v[182:183], s[26:27] op_sel_hi:[1,1,0]
	v_pk_fma_f32 v[176:177], v[168:169], v[176:177], s[28:29] op_sel_hi:[1,1,0]
	v_pk_fma_f32 v[178:179], v[170:171], v[178:179], s[28:29] op_sel_hi:[1,1,0]
	v_pk_fma_f32 v[180:181], v[172:173], v[180:181], s[28:29] op_sel_hi:[1,1,0]
	v_pk_fma_f32 v[182:183], v[174:175], v[182:183], s[28:29] op_sel_hi:[1,1,0]
	v_pk_fma_f32 v[176:177], v[168:169], v[176:177], s[30:31] op_sel_hi:[1,1,0]
	v_pk_fma_f32 v[178:179], v[170:171], v[178:179], s[30:31] op_sel_hi:[1,1,0]
	v_pk_fma_f32 v[180:181], v[172:173], v[180:181], s[30:31] op_sel_hi:[1,1,0]
	v_pk_fma_f32 v[182:183], v[174:175], v[182:183], s[30:31] op_sel_hi:[1,1,0]
	v_pk_fma_f32 v[176:177], v[168:169], v[176:177], s[34:35] op_sel_hi:[1,1,0]
	v_pk_fma_f32 v[178:179], v[170:171], v[178:179], s[34:35] op_sel_hi:[1,1,0]
	v_pk_fma_f32 v[180:181], v[172:173], v[180:181], s[34:35] op_sel_hi:[1,1,0]
	v_pk_fma_f32 v[182:183], v[174:175], v[182:183], s[34:35] op_sel_hi:[1,1,0]
	v_pk_fma_f32 v[176:177], v[168:169], v[176:177], s[36:37] op_sel_hi:[1,1,0]
	v_pk_fma_f32 v[178:179], v[170:171], v[178:179], s[36:37] op_sel_hi:[1,1,0]
	v_pk_fma_f32 v[180:181], v[172:173], v[180:181], s[36:37] op_sel_hi:[1,1,0]
	v_pk_fma_f32 v[182:183], v[174:175], v[182:183], s[36:37] op_sel_hi:[1,1,0]
	v_pk_fma_f32 v[176:177], v[168:169], v[176:177], s[38:39] op_sel_hi:[1,1,0]
	v_pk_fma_f32 v[178:179], v[170:171], v[178:179], s[38:39] op_sel_hi:[1,1,0]
	v_pk_fma_f32 v[180:181], v[172:173], v[180:181], s[38:39] op_sel_hi:[1,1,0]
	v_pk_fma_f32 v[182:183], v[174:175], v[182:183], s[38:39] op_sel_hi:[1,1,0]
	v_pk_fma_f32 v[176:177], v[168:169], v[176:177], s[40:41] op_sel_hi:[1,1,0]
	v_pk_fma_f32 v[178:179], v[170:171], v[178:179], s[40:41] op_sel_hi:[1,1,0]
	v_pk_fma_f32 v[180:181], v[172:173], v[180:181], s[40:41] op_sel_hi:[1,1,0]
	v_pk_fma_f32 v[182:183], v[174:175], v[182:183], s[40:41] op_sel_hi:[1,1,0]
	v_pk_fma_f32 v[176:177], v[168:169], v[176:177], s[42:43] op_sel_hi:[1,1,0]
	v_pk_fma_f32 v[178:179], v[170:171], v[178:179], s[42:43] op_sel_hi:[1,1,0]
	v_pk_fma_f32 v[180:181], v[172:173], v[180:181], s[42:43] op_sel_hi:[1,1,0]
	v_pk_fma_f32 v[182:183], v[174:175], v[182:183], s[42:43] op_sel_hi:[1,1,0]
	v_pk_fma_f32 v[176:177], v[168:169], v[176:177], s[44:45] op_sel_hi:[1,1,0]
	v_pk_fma_f32 v[178:179], v[170:171], v[178:179], s[44:45] op_sel_hi:[1,1,0]
	v_pk_fma_f32 v[180:181], v[172:173], v[180:181], s[44:45] op_sel_hi:[1,1,0]
	v_pk_fma_f32 v[182:183], v[174:175], v[182:183], s[44:45] op_sel_hi:[1,1,0]
	v_pk_fma_f32 v[168:169], v[168:169], v[176:177], s[48:49] op_sel_hi:[1,1,0]
	v_pk_fma_f32 v[170:171], v[170:171], v[178:179], s[48:49] op_sel_hi:[1,1,0]
	v_pk_fma_f32 v[172:173], v[172:173], v[180:181], s[48:49] op_sel_hi:[1,1,0]
	v_pk_fma_f32 v[174:175], v[174:175], v[182:183], s[48:49] op_sel_hi:[1,1,0]
	v_pk_fma_f32 v[160:161], v[160:161], v[168:169], 0.5 op_sel_hi:[1,1,0]
	v_pk_fma_f32 v[162:163], v[162:163], v[170:171], 0.5 op_sel_hi:[1,1,0]
	v_pk_fma_f32 v[164:165], v[164:165], v[172:173], 0.5 op_sel_hi:[1,1,0]
	v_pk_fma_f32 v[166:167], v[166:167], v[174:175], 0.5 op_sel_hi:[1,1,0]
	v_pk_mul_f32 v[132:133], v[132:133], v[160:161]
	v_pk_mul_f32 v[134:135], v[134:135], v[162:163]
	v_pk_mul_f32 v[128:129], v[128:129], v[164:165]
	v_pk_mul_f32 v[130:131], v[130:131], v[166:167]
	v_cvt_pk_bf16_f32 v188, v132, v133
	v_cvt_pk_bf16_f32 v189, v134, v135
	v_cvt_pk_bf16_f32 v190, v128, v129
	v_cvt_pk_bf16_f32 v191, v130, v131
	global_store_dwordx4 v[196:197], v[188:191], off offset:256
	s_and_b64 vcc, exec, s[70:71]
	s_cbranch_vccz .Lg9_nostat_0
	v_pk_add_f32 v[160:161], v[140:141], v[142:143]
	v_pk_add_f32 v[162:163], v[136:137], v[138:139]
	v_pk_add_f32 v[164:165], v[132:133], v[134:135]
	v_pk_add_f32 v[166:167], v[128:129], v[130:131]
	v_pk_mul_f32 v[168:169], v[140:141], v[140:141]
	v_pk_mul_f32 v[170:171], v[132:133], v[132:133]
	v_pk_add_f32 v[160:161], v[160:161], v[162:163]
	v_pk_add_f32 v[164:165], v[164:165], v[166:167]
	v_pk_fma_f32 v[168:169], v[142:143], v[142:143], v[168:169]
	v_pk_fma_f32 v[170:171], v[134:135], v[134:135], v[170:171]
	v_pk_fma_f32 v[168:169], v[136:137], v[136:137], v[168:169]
	v_pk_fma_f32 v[170:171], v[128:129], v[128:129], v[170:171]
	v_pk_fma_f32 v[168:169], v[138:139], v[138:139], v[168:169]
	v_pk_fma_f32 v[170:171], v[130:131], v[130:131], v[170:171]
	v_pk_add_f32 v[160:161], v[160:161], v[164:165]
	v_pk_add_f32 v[168:169], v[168:169], v[170:171]
	s_nop 0
	v_add_f32_e32 v198, v160, v161
	v_add_f32_e32 v200, v168, v169
	v_mov_b32_e32 v199, v198
	s_nop 1
	v_permlane16_swap_b32 v199, v198
	s_nop 1
	v_add_f32_e32 v198, v199, v198
	v_mov_b32_e32 v202, v198
	v_mov_b32_e32 v201, v200
	s_nop 1
	v_permlane32_swap_b32 v202, v198
	s_nop 1
	s_nop 1
	v_permlane16_swap_b32 v201, v200
	s_nop 1
	v_add_f32_e32 v199, v201, v200
	v_mov_b32_e32 v203, v199
	s_nop 1
	v_permlane32_swap_b32 v203, v199
	s_nop 1
	s_and_saveexec_b64 s[4:5], s[6:7]
	v_lshlrev_b64 v[194:195], 8, v[192:193]
	v_lshl_add_u64 v[194:195], s[16:17], 0, v[194:195]
	v_lshl_add_u64 v[194:195], s[68:69], 3, v[194:195]
	v_pk_add_f32 v[200:201], v[202:203], v[198:199]
	global_store_dwordx2 v[194:195], v[200:201], off
	s_or_b64 exec, exec, s[4:5]
.Lg9_nostat_0:
	v_add_u32_e32 v192, 0x10, v148
	v_ashrrev_i32_e32 v193, 31, v192
	v_lshlrev_b64 v[194:195], 12, v[192:193]
	v_lshl_add_u64 v[196:197], v[146:147], 0, v[194:195]
	v_pk_add_f32 v[124:125], v[124:125], v[204:205]
	v_pk_add_f32 v[126:127], v[126:127], v[206:207]
	v_pk_add_f32 v[120:121], v[120:121], v[208:209]
	v_pk_add_f32 v[122:123], v[122:123], v[210:211]
	v_med3_f32 v160, v124, s78, v158
	v_med3_f32 v161, v125, s78, v158
	v_med3_f32 v162, v126, s78, v158
	v_med3_f32 v163, v127, s78, v158
	v_med3_f32 v164, v120, s78, v158
	v_med3_f32 v165, v121, s78, v158
	v_med3_f32 v166, v122, s78, v158
	v_med3_f32 v167, v123, s78, v158
	v_pk_mul_f32 v[168:169], v[160:161], v[160:161]
	v_pk_mul_f32 v[170:171], v[162:163], v[162:163]
	v_pk_mul_f32 v[172:173], v[164:165], v[164:165]
	v_pk_mul_f32 v[174:175], v[166:167], v[166:167]
	v_pk_fma_f32 v[168:169], v[168:169], s[20:21], -1.0 op_sel_hi:[1,0,0]
	v_pk_fma_f32 v[170:171], v[170:171], s[20:21], -1.0 op_sel_hi:[1,0,0]
	v_pk_fma_f32 v[172:173], v[172:173], s[20:21], -1.0 op_sel_hi:[1,0,0]
	v_pk_fma_f32 v[174:175], v[174:175], s[20:21], -1.0 op_sel_hi:[1,0,0]
	v_pk_fma_f32 v[176:177], v[168:169], s[22:23], v[150:151] op_sel_hi:[1,0,0] neg_lo:[1,0,0] neg_hi:[1,0,0]
	v_pk_fma_f32 v[178:179], v[170:171], s[22:23], v[150:151] op_sel_hi:[1,0,0] neg_lo:[1,0,0] neg_hi:[1,0,0]
	v_pk_fma_f32 v[180:181], v[172:173], s[22:23], v[150:151] op_sel_hi:[1,0,0] neg_lo:[1,0,0] neg_hi:[1,0,0]
	v_pk_fma_f32 v[182:183], v[174:175], s[22:23], v[150:151] op_sel_hi:[1,0,0] neg_lo:[1,0,0] neg_hi:[1,0,0]
	v_pk_fma_f32 v[176:177], v[168:169], v[176:177], s[26:27] op_sel_hi:[1,1,0]
	v_pk_fma_f32 v[178:179], v[170:171], v[178:179], s[26:27] op_sel_hi:[1,1,0]
	v_pk_fma_f32 v[180:181], v[172:173], v[180:181], s[26:27] op_sel_hi:[1,1,0]
	v_pk_fma_f32 v[182:183], v[174:175], v[182:183], s[26:27] op_sel_hi:[1,1,0]
	v_pk_fma_f32 v[176:177], v[168:169], v[176:177], s[28:29] op_sel_hi:[1,1,0]
	v_pk_fma_f32 v[178:179], v[170:171], v[178:179], s[28:29] op_sel_hi:[1,1,0]
	v_pk_fma_f32 v[180:181], v[172:173], v[180:181], s[28:29] op_sel_hi:[1,1,0]
	v_pk_fma_f32 v[182:183], v[174:175], v[182:183], s[28:29] op_sel_hi:[1,1,0]
	v_pk_fma_f32 v[176:177], v[168:169], v[176:177], s[30:31] op_sel_hi:[1,1,0]
	v_pk_fma_f32 v[178:179], v[170:171], v[178:179], s[30:31] op_sel_hi:[1,1,0]
	v_pk_fma_f32 v[180:181], v[172:173], v[180:181], s[30:31] op_sel_hi:[1,1,0]
	v_pk_fma_f32 v[182:183], v[174:175], v[182:183], s[30:31] op_sel_hi:[1,1,0]
	v_pk_fma_f32 v[176:177], v[168:169], v[176:177], s[34:35] op_sel_hi:[1,1,0]
	v_pk_fma_f32 v[178:179], v[170:171], v[178:179], s[34:35] op_sel_hi:[1,1,0]
	v_pk_fma_f32 v[180:181], v[172:173], v[180:181], s[34:35] op_sel_hi:[1,1,0]
	v_pk_fma_f32 v[182:183], v[174:175], v[182:183], s[34:35] op_sel_hi:[1,1,0]
	v_pk_fma_f32 v[176:177], v[168:169], v[176:177], s[36:37] op_sel_hi:[1,1,0]
	v_pk_fma_f32 v[178:179], v[170:171], v[178:179], s[36:37] op_sel_hi:[1,1,0]
	v_pk_fma_f32 v[180:181], v[172:173], v[180:181], s[36:37] op_sel_hi:[1,1,0]
	v_pk_fma_f32 v[182:183], v[174:175], v[182:183], s[36:37] op_sel_hi:[1,1,0]
	v_pk_fma_f32 v[176:177], v[168:169], v[176:177], s[38:39] op_sel_hi:[1,1,0]
	v_pk_fma_f32 v[178:179], v[170:171], v[178:179], s[38:39] op_sel_hi:[1,1,0]
	v_pk_fma_f32 v[180:181], v[172:173], v[180:181], s[38:39] op_sel_hi:[1,1,0]
	v_pk_fma_f32 v[182:183], v[174:175], v[182:183], s[38:39] op_sel_hi:[1,1,0]
	v_pk_fma_f32 v[176:177], v[168:169], v[176:177], s[40:41] op_sel_hi:[1,1,0]
	v_pk_fma_f32 v[178:179], v[170:171], v[178:179], s[40:41] op_sel_hi:[1,1,0]
	v_pk_fma_f32 v[180:181], v[172:173], v[180:181], s[40:41] op_sel_hi:[1,1,0]
	v_pk_fma_f32 v[182:183], v[174:175], v[182:183], s[40:41] op_sel_hi:[1,1,0]
	v_pk_fma_f32 v[176:177], v[168:169], v[176:177], s[42:43] op_sel_hi:[1,1,0]
	v_pk_fma_f32 v[178:179], v[170:171], v[178:179], s[42:43] op_sel_hi:[1,1,0]
	v_pk_fma_f32 v[180:181], v[172:173], v[180:181], s[42:43] op_sel_hi:[1,1,0]
	v_pk_fma_f32 v[182:183], v[174:175], v[182:183], s[42:43] op_sel_hi:[1,1,0]
	v_pk_fma_f32 v[176:177], v[168:169], v[176:177], s[44:45] op_sel_hi:[1,1,0]
	v_pk_fma_f32 v[178:179], v[170:171], v[178:179], s[44:45] op_sel_hi:[1,1,0]
	v_pk_fma_f32 v[180:181], v[172:173], v[180:181], s[44:45] op_sel_hi:[1,1,0]
	v_pk_fma_f32 v[182:183], v[174:175], v[182:183], s[44:45] op_sel_hi:[1,1,0]
	v_pk_fma_f32 v[168:169], v[168:169], v[176:177], s[48:49] op_sel_hi:[1,1,0]
	v_pk_fma_f32 v[170:171], v[170:171], v[178:179], s[48:49] op_sel_hi:[1,1,0]
	v_pk_fma_f32 v[172:173], v[172:173], v[180:181], s[48:49] op_sel_hi:[1,1,0]
	v_pk_fma_f32 v[174:175], v[174:175], v[182:183], s[48:49] op_sel_hi:[1,1,0]
	v_pk_fma_f32 v[160:161], v[160:161], v[168:169], 0.5 op_sel_hi:[1,1,0]
	v_pk_fma_f32 v[162:163], v[162:163], v[170:171], 0.5 op_sel_hi:[1,1,0]
	v_pk_fma_f32 v[164:165], v[164:165], v[172:173], 0.5 op_sel_hi:[1,1,0]
	v_pk_fma_f32 v[166:167], v[166:167], v[174:175], 0.5 op_sel_hi:[1,1,0]
	v_pk_mul_f32 v[124:125], v[124:125], v[160:161]
	v_pk_mul_f32 v[126:127], v[126:127], v[162:163]
	v_pk_mul_f32 v[120:121], v[120:121], v[164:165]
	v_pk_mul_f32 v[122:123], v[122:123], v[166:167]
	v_cvt_pk_bf16_f32 v184, v124, v125
	v_cvt_pk_bf16_f32 v185, v126, v127
	v_cvt_pk_bf16_f32 v186, v120, v121
	v_cvt_pk_bf16_f32 v187, v122, v123
	global_store_dwordx4 v[196:197], v[184:187], off
	v_pk_add_f32 v[116:117], v[116:117], v[212:213]
	v_pk_add_f32 v[118:119], v[118:119], v[214:215]
	v_pk_add_f32 v[112:113], v[112:113], v[216:217]
	v_pk_add_f32 v[114:115], v[114:115], v[218:219]
	v_med3_f32 v160, v116, s78, v158
	v_med3_f32 v161, v117, s78, v158
	v_med3_f32 v162, v118, s78, v158
	v_med3_f32 v163, v119, s78, v158
	v_med3_f32 v164, v112, s78, v158
	v_med3_f32 v165, v113, s78, v158
	v_med3_f32 v166, v114, s78, v158
	v_med3_f32 v167, v115, s78, v158
	v_pk_mul_f32 v[168:169], v[160:161], v[160:161]
	v_pk_mul_f32 v[170:171], v[162:163], v[162:163]
	v_pk_mul_f32 v[172:173], v[164:165], v[164:165]
	v_pk_mul_f32 v[174:175], v[166:167], v[166:167]
	v_pk_fma_f32 v[168:169], v[168:169], s[20:21], -1.0 op_sel_hi:[1,0,0]
	v_pk_fma_f32 v[170:171], v[170:171], s[20:21], -1.0 op_sel_hi:[1,0,0]
	v_pk_fma_f32 v[172:173], v[172:173], s[20:21], -1.0 op_sel_hi:[1,0,0]
	v_pk_fma_f32 v[174:175], v[174:175], s[20:21], -1.0 op_sel_hi:[1,0,0]
	v_pk_fma_f32 v[176:177], v[168:169], s[22:23], v[150:151] op_sel_hi:[1,0,0] neg_lo:[1,0,0] neg_hi:[1,0,0]
	v_pk_fma_f32 v[178:179], v[170:171], s[22:23], v[150:151] op_sel_hi:[1,0,0] neg_lo:[1,0,0] neg_hi:[1,0,0]
	v_pk_fma_f32 v[180:181], v[172:173], s[22:23], v[150:151] op_sel_hi:[1,0,0] neg_lo:[1,0,0] neg_hi:[1,0,0]
	v_pk_fma_f32 v[182:183], v[174:175], s[22:23], v[150:151] op_sel_hi:[1,0,0] neg_lo:[1,0,0] neg_hi:[1,0,0]
	v_pk_fma_f32 v[176:177], v[168:169], v[176:177], s[26:27] op_sel_hi:[1,1,0]
	v_pk_fma_f32 v[178:179], v[170:171], v[178:179], s[26:27] op_sel_hi:[1,1,0]
	v_pk_fma_f32 v[180:181], v[172:173], v[180:181], s[26:27] op_sel_hi:[1,1,0]
	v_pk_fma_f32 v[182:183], v[174:175], v[182:183], s[26:27] op_sel_hi:[1,1,0]
	v_pk_fma_f32 v[176:177], v[168:169], v[176:177], s[28:29] op_sel_hi:[1,1,0]
	v_pk_fma_f32 v[178:179], v[170:171], v[178:179], s[28:29] op_sel_hi:[1,1,0]
	v_pk_fma_f32 v[180:181], v[172:173], v[180:181], s[28:29] op_sel_hi:[1,1,0]
	v_pk_fma_f32 v[182:183], v[174:175], v[182:183], s[28:29] op_sel_hi:[1,1,0]
	v_pk_fma_f32 v[176:177], v[168:169], v[176:177], s[30:31] op_sel_hi:[1,1,0]
	v_pk_fma_f32 v[178:179], v[170:171], v[178:179], s[30:31] op_sel_hi:[1,1,0]
	v_pk_fma_f32 v[180:181], v[172:173], v[180:181], s[30:31] op_sel_hi:[1,1,0]
	v_pk_fma_f32 v[182:183], v[174:175], v[182:183], s[30:31] op_sel_hi:[1,1,0]
	v_pk_fma_f32 v[176:177], v[168:169], v[176:177], s[34:35] op_sel_hi:[1,1,0]
	v_pk_fma_f32 v[178:179], v[170:171], v[178:179], s[34:35] op_sel_hi:[1,1,0]
	v_pk_fma_f32 v[180:181], v[172:173], v[180:181], s[34:35] op_sel_hi:[1,1,0]
	v_pk_fma_f32 v[182:183], v[174:175], v[182:183], s[34:35] op_sel_hi:[1,1,0]
	v_pk_fma_f32 v[176:177], v[168:169], v[176:177], s[36:37] op_sel_hi:[1,1,0]
	v_pk_fma_f32 v[178:179], v[170:171], v[178:179], s[36:37] op_sel_hi:[1,1,0]
	v_pk_fma_f32 v[180:181], v[172:173], v[180:181], s[36:37] op_sel_hi:[1,1,0]
	v_pk_fma_f32 v[182:183], v[174:175], v[182:183], s[36:37] op_sel_hi:[1,1,0]
	v_pk_fma_f32 v[176:177], v[168:169], v[176:177], s[38:39] op_sel_hi:[1,1,0]
	v_pk_fma_f32 v[178:179], v[170:171], v[178:179], s[38:39] op_sel_hi:[1,1,0]
	v_pk_fma_f32 v[180:181], v[172:173], v[180:181], s[38:39] op_sel_hi:[1,1,0]
	v_pk_fma_f32 v[182:183], v[174:175], v[182:183], s[38:39] op_sel_hi:[1,1,0]
	v_pk_fma_f32 v[176:177], v[168:169], v[176:177], s[40:41] op_sel_hi:[1,1,0]
	v_pk_fma_f32 v[178:179], v[170:171], v[178:179], s[40:41] op_sel_hi:[1,1,0]
	v_pk_fma_f32 v[180:181], v[172:173], v[180:181], s[40:41] op_sel_hi:[1,1,0]
	v_pk_fma_f32 v[182:183], v[174:175], v[182:183], s[40:41] op_sel_hi:[1,1,0]
	v_pk_fma_f32 v[176:177], v[168:169], v[176:177], s[42:43] op_sel_hi:[1,1,0]
	v_pk_fma_f32 v[178:179], v[170:171], v[178:179], s[42:43] op_sel_hi:[1,1,0]
	v_pk_fma_f32 v[180:181], v[172:173], v[180:181], s[42:43] op_sel_hi:[1,1,0]
	v_pk_fma_f32 v[182:183], v[174:175], v[182:183], s[42:43] op_sel_hi:[1,1,0]
	v_pk_fma_f32 v[176:177], v[168:169], v[176:177], s[44:45] op_sel_hi:[1,1,0]
	v_pk_fma_f32 v[178:179], v[170:171], v[178:179], s[44:45] op_sel_hi:[1,1,0]
	v_pk_fma_f32 v[180:181], v[172:173], v[180:181], s[44:45] op_sel_hi:[1,1,0]
	v_pk_fma_f32 v[182:183], v[174:175], v[182:183], s[44:45] op_sel_hi:[1,1,0]
	v_pk_fma_f32 v[168:169], v[168:169], v[176:177], s[48:49] op_sel_hi:[1,1,0]
	v_pk_fma_f32 v[170:171], v[170:171], v[178:179], s[48:49] op_sel_hi:[1,1,0]
	v_pk_fma_f32 v[172:173], v[172:173], v[180:181], s[48:49] op_sel_hi:[1,1,0]
	v_pk_fma_f32 v[174:175], v[174:175], v[182:183], s[48:49] op_sel_hi:[1,1,0]
	v_pk_fma_f32 v[160:161], v[160:161], v[168:169], 0.5 op_sel_hi:[1,1,0]
	v_pk_fma_f32 v[162:163], v[162:163], v[170:171], 0.5 op_sel_hi:[1,1,0]
	v_pk_fma_f32 v[164:165], v[164:165], v[172:173], 0.5 op_sel_hi:[1,1,0]
	v_pk_fma_f32 v[166:167], v[166:167], v[174:175], 0.5 op_sel_hi:[1,1,0]
	v_pk_mul_f32 v[116:117], v[116:117], v[160:161]
	v_pk_mul_f32 v[118:119], v[118:119], v[162:163]
	v_pk_mul_f32 v[112:113], v[112:113], v[164:165]
	v_pk_mul_f32 v[114:115], v[114:115], v[166:167]
	v_cvt_pk_bf16_f32 v188, v116, v117
	v_cvt_pk_bf16_f32 v189, v118, v119
	v_cvt_pk_bf16_f32 v190, v112, v113
	v_cvt_pk_bf16_f32 v191, v114, v115
	global_store_dwordx4 v[196:197], v[188:191], off offset:256
	s_and_b64 vcc, exec, s[70:71]
	s_cbranch_vccz .Lg9_nostat_1
	v_pk_add_f32 v[160:161], v[124:125], v[126:127]
	v_pk_add_f32 v[162:163], v[120:121], v[122:123]
	v_pk_add_f32 v[164:165], v[116:117], v[118:119]
	v_pk_add_f32 v[166:167], v[112:113], v[114:115]
	v_pk_mul_f32 v[168:169], v[124:125], v[124:125]
	v_pk_mul_f32 v[170:171], v[116:117], v[116:117]
	v_pk_add_f32 v[160:161], v[160:161], v[162:163]
	v_pk_add_f32 v[164:165], v[164:165], v[166:167]
	v_pk_fma_f32 v[168:169], v[126:127], v[126:127], v[168:169]
	v_pk_fma_f32 v[170:171], v[118:119], v[118:119], v[170:171]
	v_pk_fma_f32 v[168:169], v[120:121], v[120:121], v[168:169]
	v_pk_fma_f32 v[170:171], v[112:113], v[112:113], v[170:171]
	v_pk_fma_f32 v[168:169], v[122:123], v[122:123], v[168:169]
	v_pk_fma_f32 v[170:171], v[114:115], v[114:115], v[170:171]
	v_pk_add_f32 v[160:161], v[160:161], v[164:165]
	v_pk_add_f32 v[168:169], v[168:169], v[170:171]
	s_nop 0
	v_add_f32_e32 v198, v160, v161
	v_add_f32_e32 v200, v168, v169
	v_mov_b32_e32 v199, v198
	s_nop 1
	v_permlane16_swap_b32 v199, v198
	s_nop 1
	v_add_f32_e32 v198, v199, v198
	v_mov_b32_e32 v202, v198
	v_mov_b32_e32 v201, v200
	s_nop 1
	v_permlane32_swap_b32 v202, v198
	s_nop 1
	s_nop 1
	v_permlane16_swap_b32 v201, v200
	s_nop 1
	v_add_f32_e32 v199, v201, v200
	v_mov_b32_e32 v203, v199
	s_nop 1
	v_permlane32_swap_b32 v203, v199
	s_nop 1
	s_and_saveexec_b64 s[4:5], s[6:7]
	v_lshlrev_b64 v[194:195], 8, v[192:193]
	v_lshl_add_u64 v[194:195], s[16:17], 0, v[194:195]
	v_lshl_add_u64 v[194:195], s[68:69], 3, v[194:195]
	v_pk_add_f32 v[200:201], v[202:203], v[198:199]
	global_store_dwordx2 v[194:195], v[200:201], off
	s_or_b64 exec, exec, s[4:5]
.Lg9_nostat_1:
	v_add_u32_e32 v192, 0x20, v148
	v_ashrrev_i32_e32 v193, 31, v192
	v_lshlrev_b64 v[194:195], 12, v[192:193]
	v_lshl_add_u64 v[196:197], v[146:147], 0, v[194:195]
	v_pk_add_f32 v[108:109], v[108:109], v[204:205]
	v_pk_add_f32 v[110:111], v[110:111], v[206:207]
	v_pk_add_f32 v[104:105], v[104:105], v[208:209]
	v_pk_add_f32 v[106:107], v[106:107], v[210:211]
	v_med3_f32 v160, v108, s78, v158
	v_med3_f32 v161, v109, s78, v158
	v_med3_f32 v162, v110, s78, v158
	v_med3_f32 v163, v111, s78, v158
	v_med3_f32 v164, v104, s78, v158
	v_med3_f32 v165, v105, s78, v158
	v_med3_f32 v166, v106, s78, v158
	v_med3_f32 v167, v107, s78, v158
	v_pk_mul_f32 v[168:169], v[160:161], v[160:161]
	v_pk_mul_f32 v[170:171], v[162:163], v[162:163]
	v_pk_mul_f32 v[172:173], v[164:165], v[164:165]
	v_pk_mul_f32 v[174:175], v[166:167], v[166:167]
	v_pk_fma_f32 v[168:169], v[168:169], s[20:21], -1.0 op_sel_hi:[1,0,0]
	v_pk_fma_f32 v[170:171], v[170:171], s[20:21], -1.0 op_sel_hi:[1,0,0]
	v_pk_fma_f32 v[172:173], v[172:173], s[20:21], -1.0 op_sel_hi:[1,0,0]
	v_pk_fma_f32 v[174:175], v[174:175], s[20:21], -1.0 op_sel_hi:[1,0,0]
	v_pk_fma_f32 v[176:177], v[168:169], s[22:23], v[150:151] op_sel_hi:[1,0,0] neg_lo:[1,0,0] neg_hi:[1,0,0]
	v_pk_fma_f32 v[178:179], v[170:171], s[22:23], v[150:151] op_sel_hi:[1,0,0] neg_lo:[1,0,0] neg_hi:[1,0,0]
	v_pk_fma_f32 v[180:181], v[172:173], s[22:23], v[150:151] op_sel_hi:[1,0,0] neg_lo:[1,0,0] neg_hi:[1,0,0]
	v_pk_fma_f32 v[182:183], v[174:175], s[22:23], v[150:151] op_sel_hi:[1,0,0] neg_lo:[1,0,0] neg_hi:[1,0,0]
	v_pk_fma_f32 v[176:177], v[168:169], v[176:177], s[26:27] op_sel_hi:[1,1,0]
	v_pk_fma_f32 v[178:179], v[170:171], v[178:179], s[26:27] op_sel_hi:[1,1,0]
	v_pk_fma_f32 v[180:181], v[172:173], v[180:181], s[26:27] op_sel_hi:[1,1,0]
	v_pk_fma_f32 v[182:183], v[174:175], v[182:183], s[26:27] op_sel_hi:[1,1,0]
	v_pk_fma_f32 v[176:177], v[168:169], v[176:177], s[28:29] op_sel_hi:[1,1,0]
	v_pk_fma_f32 v[178:179], v[170:171], v[178:179], s[28:29] op_sel_hi:[1,1,0]
	v_pk_fma_f32 v[180:181], v[172:173], v[180:181], s[28:29] op_sel_hi:[1,1,0]
	v_pk_fma_f32 v[182:183], v[174:175], v[182:183], s[28:29] op_sel_hi:[1,1,0]
	v_pk_fma_f32 v[176:177], v[168:169], v[176:177], s[30:31] op_sel_hi:[1,1,0]
	v_pk_fma_f32 v[178:179], v[170:171], v[178:179], s[30:31] op_sel_hi:[1,1,0]
	v_pk_fma_f32 v[180:181], v[172:173], v[180:181], s[30:31] op_sel_hi:[1,1,0]
	v_pk_fma_f32 v[182:183], v[174:175], v[182:183], s[30:31] op_sel_hi:[1,1,0]
	v_pk_fma_f32 v[176:177], v[168:169], v[176:177], s[34:35] op_sel_hi:[1,1,0]
	v_pk_fma_f32 v[178:179], v[170:171], v[178:179], s[34:35] op_sel_hi:[1,1,0]
	v_pk_fma_f32 v[180:181], v[172:173], v[180:181], s[34:35] op_sel_hi:[1,1,0]
	v_pk_fma_f32 v[182:183], v[174:175], v[182:183], s[34:35] op_sel_hi:[1,1,0]
	v_pk_fma_f32 v[176:177], v[168:169], v[176:177], s[36:37] op_sel_hi:[1,1,0]
	v_pk_fma_f32 v[178:179], v[170:171], v[178:179], s[36:37] op_sel_hi:[1,1,0]
	v_pk_fma_f32 v[180:181], v[172:173], v[180:181], s[36:37] op_sel_hi:[1,1,0]
	v_pk_fma_f32 v[182:183], v[174:175], v[182:183], s[36:37] op_sel_hi:[1,1,0]
	v_pk_fma_f32 v[176:177], v[168:169], v[176:177], s[38:39] op_sel_hi:[1,1,0]
	v_pk_fma_f32 v[178:179], v[170:171], v[178:179], s[38:39] op_sel_hi:[1,1,0]
	v_pk_fma_f32 v[180:181], v[172:173], v[180:181], s[38:39] op_sel_hi:[1,1,0]
	v_pk_fma_f32 v[182:183], v[174:175], v[182:183], s[38:39] op_sel_hi:[1,1,0]
	v_pk_fma_f32 v[176:177], v[168:169], v[176:177], s[40:41] op_sel_hi:[1,1,0]
	v_pk_fma_f32 v[178:179], v[170:171], v[178:179], s[40:41] op_sel_hi:[1,1,0]
	v_pk_fma_f32 v[180:181], v[172:173], v[180:181], s[40:41] op_sel_hi:[1,1,0]
	v_pk_fma_f32 v[182:183], v[174:175], v[182:183], s[40:41] op_sel_hi:[1,1,0]
	v_pk_fma_f32 v[176:177], v[168:169], v[176:177], s[42:43] op_sel_hi:[1,1,0]
	v_pk_fma_f32 v[178:179], v[170:171], v[178:179], s[42:43] op_sel_hi:[1,1,0]
	v_pk_fma_f32 v[180:181], v[172:173], v[180:181], s[42:43] op_sel_hi:[1,1,0]
	v_pk_fma_f32 v[182:183], v[174:175], v[182:183], s[42:43] op_sel_hi:[1,1,0]
	v_pk_fma_f32 v[176:177], v[168:169], v[176:177], s[44:45] op_sel_hi:[1,1,0]
	v_pk_fma_f32 v[178:179], v[170:171], v[178:179], s[44:45] op_sel_hi:[1,1,0]
	v_pk_fma_f32 v[180:181], v[172:173], v[180:181], s[44:45] op_sel_hi:[1,1,0]
	v_pk_fma_f32 v[182:183], v[174:175], v[182:183], s[44:45] op_sel_hi:[1,1,0]
	v_pk_fma_f32 v[168:169], v[168:169], v[176:177], s[48:49] op_sel_hi:[1,1,0]
	v_pk_fma_f32 v[170:171], v[170:171], v[178:179], s[48:49] op_sel_hi:[1,1,0]
	v_pk_fma_f32 v[172:173], v[172:173], v[180:181], s[48:49] op_sel_hi:[1,1,0]
	v_pk_fma_f32 v[174:175], v[174:175], v[182:183], s[48:49] op_sel_hi:[1,1,0]
	v_pk_fma_f32 v[160:161], v[160:161], v[168:169], 0.5 op_sel_hi:[1,1,0]
	v_pk_fma_f32 v[162:163], v[162:163], v[170:171], 0.5 op_sel_hi:[1,1,0]
	v_pk_fma_f32 v[164:165], v[164:165], v[172:173], 0.5 op_sel_hi:[1,1,0]
	v_pk_fma_f32 v[166:167], v[166:167], v[174:175], 0.5 op_sel_hi:[1,1,0]
	v_pk_mul_f32 v[108:109], v[108:109], v[160:161]
	v_pk_mul_f32 v[110:111], v[110:111], v[162:163]
	v_pk_mul_f32 v[104:105], v[104:105], v[164:165]
	v_pk_mul_f32 v[106:107], v[106:107], v[166:167]
	v_cvt_pk_bf16_f32 v184, v108, v109
	v_cvt_pk_bf16_f32 v185, v110, v111
	v_cvt_pk_bf16_f32 v186, v104, v105
	v_cvt_pk_bf16_f32 v187, v106, v107
	global_store_dwordx4 v[196:197], v[184:187], off
	v_pk_add_f32 v[100:101], v[100:101], v[212:213]
	v_pk_add_f32 v[102:103], v[102:103], v[214:215]
	v_pk_add_f32 v[96:97], v[96:97], v[216:217]
	v_pk_add_f32 v[98:99], v[98:99], v[218:219]
	v_med3_f32 v160, v100, s78, v158
	v_med3_f32 v161, v101, s78, v158
	v_med3_f32 v162, v102, s78, v158
	v_med3_f32 v163, v103, s78, v158
	v_med3_f32 v164, v96, s78, v158
	v_med3_f32 v165, v97, s78, v158
	v_med3_f32 v166, v98, s78, v158
	v_med3_f32 v167, v99, s78, v158
	v_pk_mul_f32 v[168:169], v[160:161], v[160:161]
	v_pk_mul_f32 v[170:171], v[162:163], v[162:163]
	v_pk_mul_f32 v[172:173], v[164:165], v[164:165]
	v_pk_mul_f32 v[174:175], v[166:167], v[166:167]
	v_pk_fma_f32 v[168:169], v[168:169], s[20:21], -1.0 op_sel_hi:[1,0,0]
	v_pk_fma_f32 v[170:171], v[170:171], s[20:21], -1.0 op_sel_hi:[1,0,0]
	v_pk_fma_f32 v[172:173], v[172:173], s[20:21], -1.0 op_sel_hi:[1,0,0]
	v_pk_fma_f32 v[174:175], v[174:175], s[20:21], -1.0 op_sel_hi:[1,0,0]
	v_pk_fma_f32 v[176:177], v[168:169], s[22:23], v[150:151] op_sel_hi:[1,0,0] neg_lo:[1,0,0] neg_hi:[1,0,0]
	v_pk_fma_f32 v[178:179], v[170:171], s[22:23], v[150:151] op_sel_hi:[1,0,0] neg_lo:[1,0,0] neg_hi:[1,0,0]
	v_pk_fma_f32 v[180:181], v[172:173], s[22:23], v[150:151] op_sel_hi:[1,0,0] neg_lo:[1,0,0] neg_hi:[1,0,0]
	v_pk_fma_f32 v[182:183], v[174:175], s[22:23], v[150:151] op_sel_hi:[1,0,0] neg_lo:[1,0,0] neg_hi:[1,0,0]
	v_pk_fma_f32 v[176:177], v[168:169], v[176:177], s[26:27] op_sel_hi:[1,1,0]
	v_pk_fma_f32 v[178:179], v[170:171], v[178:179], s[26:27] op_sel_hi:[1,1,0]
	v_pk_fma_f32 v[180:181], v[172:173], v[180:181], s[26:27] op_sel_hi:[1,1,0]
	v_pk_fma_f32 v[182:183], v[174:175], v[182:183], s[26:27] op_sel_hi:[1,1,0]
	v_pk_fma_f32 v[176:177], v[168:169], v[176:177], s[28:29] op_sel_hi:[1,1,0]
	v_pk_fma_f32 v[178:179], v[170:171], v[178:179], s[28:29] op_sel_hi:[1,1,0]
	v_pk_fma_f32 v[180:181], v[172:173], v[180:181], s[28:29] op_sel_hi:[1,1,0]
	v_pk_fma_f32 v[182:183], v[174:175], v[182:183], s[28:29] op_sel_hi:[1,1,0]
	v_pk_fma_f32 v[176:177], v[168:169], v[176:177], s[30:31] op_sel_hi:[1,1,0]
	v_pk_fma_f32 v[178:179], v[170:171], v[178:179], s[30:31] op_sel_hi:[1,1,0]
	v_pk_fma_f32 v[180:181], v[172:173], v[180:181], s[30:31] op_sel_hi:[1,1,0]
	v_pk_fma_f32 v[182:183], v[174:175], v[182:183], s[30:31] op_sel_hi:[1,1,0]
	v_pk_fma_f32 v[176:177], v[168:169], v[176:177], s[34:35] op_sel_hi:[1,1,0]
	v_pk_fma_f32 v[178:179], v[170:171], v[178:179], s[34:35] op_sel_hi:[1,1,0]
	v_pk_fma_f32 v[180:181], v[172:173], v[180:181], s[34:35] op_sel_hi:[1,1,0]
	v_pk_fma_f32 v[182:183], v[174:175], v[182:183], s[34:35] op_sel_hi:[1,1,0]
	v_pk_fma_f32 v[176:177], v[168:169], v[176:177], s[36:37] op_sel_hi:[1,1,0]
	v_pk_fma_f32 v[178:179], v[170:171], v[178:179], s[36:37] op_sel_hi:[1,1,0]
	v_pk_fma_f32 v[180:181], v[172:173], v[180:181], s[36:37] op_sel_hi:[1,1,0]
	v_pk_fma_f32 v[182:183], v[174:175], v[182:183], s[36:37] op_sel_hi:[1,1,0]
	v_pk_fma_f32 v[176:177], v[168:169], v[176:177], s[38:39] op_sel_hi:[1,1,0]
	v_pk_fma_f32 v[178:179], v[170:171], v[178:179], s[38:39] op_sel_hi:[1,1,0]
	v_pk_fma_f32 v[180:181], v[172:173], v[180:181], s[38:39] op_sel_hi:[1,1,0]
	v_pk_fma_f32 v[182:183], v[174:175], v[182:183], s[38:39] op_sel_hi:[1,1,0]
	v_pk_fma_f32 v[176:177], v[168:169], v[176:177], s[40:41] op_sel_hi:[1,1,0]
	v_pk_fma_f32 v[178:179], v[170:171], v[178:179], s[40:41] op_sel_hi:[1,1,0]
	v_pk_fma_f32 v[180:181], v[172:173], v[180:181], s[40:41] op_sel_hi:[1,1,0]
	v_pk_fma_f32 v[182:183], v[174:175], v[182:183], s[40:41] op_sel_hi:[1,1,0]
	v_pk_fma_f32 v[176:177], v[168:169], v[176:177], s[42:43] op_sel_hi:[1,1,0]
	v_pk_fma_f32 v[178:179], v[170:171], v[178:179], s[42:43] op_sel_hi:[1,1,0]
	v_pk_fma_f32 v[180:181], v[172:173], v[180:181], s[42:43] op_sel_hi:[1,1,0]
	v_pk_fma_f32 v[182:183], v[174:175], v[182:183], s[42:43] op_sel_hi:[1,1,0]
	v_pk_fma_f32 v[176:177], v[168:169], v[176:177], s[44:45] op_sel_hi:[1,1,0]
	v_pk_fma_f32 v[178:179], v[170:171], v[178:179], s[44:45] op_sel_hi:[1,1,0]
	v_pk_fma_f32 v[180:181], v[172:173], v[180:181], s[44:45] op_sel_hi:[1,1,0]
	v_pk_fma_f32 v[182:183], v[174:175], v[182:183], s[44:45] op_sel_hi:[1,1,0]
	v_pk_fma_f32 v[168:169], v[168:169], v[176:177], s[48:49] op_sel_hi:[1,1,0]
	v_pk_fma_f32 v[170:171], v[170:171], v[178:179], s[48:49] op_sel_hi:[1,1,0]
	v_pk_fma_f32 v[172:173], v[172:173], v[180:181], s[48:49] op_sel_hi:[1,1,0]
	v_pk_fma_f32 v[174:175], v[174:175], v[182:183], s[48:49] op_sel_hi:[1,1,0]
	v_pk_fma_f32 v[160:161], v[160:161], v[168:169], 0.5 op_sel_hi:[1,1,0]
	v_pk_fma_f32 v[162:163], v[162:163], v[170:171], 0.5 op_sel_hi:[1,1,0]
	v_pk_fma_f32 v[164:165], v[164:165], v[172:173], 0.5 op_sel_hi:[1,1,0]
	v_pk_fma_f32 v[166:167], v[166:167], v[174:175], 0.5 op_sel_hi:[1,1,0]
	v_pk_mul_f32 v[100:101], v[100:101], v[160:161]
	v_pk_mul_f32 v[102:103], v[102:103], v[162:163]
	v_pk_mul_f32 v[96:97], v[96:97], v[164:165]
	v_pk_mul_f32 v[98:99], v[98:99], v[166:167]
	v_cvt_pk_bf16_f32 v188, v100, v101
	v_cvt_pk_bf16_f32 v189, v102, v103
	v_cvt_pk_bf16_f32 v190, v96, v97
	v_cvt_pk_bf16_f32 v191, v98, v99
	global_store_dwordx4 v[196:197], v[188:191], off offset:256
	s_and_b64 vcc, exec, s[70:71]
	s_cbranch_vccz .Lg9_nostat_2
	v_pk_add_f32 v[160:161], v[108:109], v[110:111]
	v_pk_add_f32 v[162:163], v[104:105], v[106:107]
	v_pk_add_f32 v[164:165], v[100:101], v[102:103]
	v_pk_add_f32 v[166:167], v[96:97], v[98:99]
	v_pk_mul_f32 v[168:169], v[108:109], v[108:109]
	v_pk_mul_f32 v[170:171], v[100:101], v[100:101]
	v_pk_add_f32 v[160:161], v[160:161], v[162:163]
	v_pk_add_f32 v[164:165], v[164:165], v[166:167]
	v_pk_fma_f32 v[168:169], v[110:111], v[110:111], v[168:169]
	v_pk_fma_f32 v[170:171], v[102:103], v[102:103], v[170:171]
	v_pk_fma_f32 v[168:169], v[104:105], v[104:105], v[168:169]
	v_pk_fma_f32 v[170:171], v[96:97], v[96:97], v[170:171]
	v_pk_fma_f32 v[168:169], v[106:107], v[106:107], v[168:169]
	v_pk_fma_f32 v[170:171], v[98:99], v[98:99], v[170:171]
	v_pk_add_f32 v[160:161], v[160:161], v[164:165]
	v_pk_add_f32 v[168:169], v[168:169], v[170:171]
	s_nop 0
	v_add_f32_e32 v198, v160, v161
	v_add_f32_e32 v200, v168, v169
	v_mov_b32_e32 v199, v198
	s_nop 1
	v_permlane16_swap_b32 v199, v198
	s_nop 1
	v_add_f32_e32 v198, v199, v198
	v_mov_b32_e32 v202, v198
	v_mov_b32_e32 v201, v200
	s_nop 1
	v_permlane32_swap_b32 v202, v198
	s_nop 1
	s_nop 1
	v_permlane16_swap_b32 v201, v200
	s_nop 1
	v_add_f32_e32 v199, v201, v200
	v_mov_b32_e32 v203, v199
	s_nop 1
	v_permlane32_swap_b32 v203, v199
	s_nop 1
	s_and_saveexec_b64 s[4:5], s[6:7]
	v_lshlrev_b64 v[194:195], 8, v[192:193]
	v_lshl_add_u64 v[194:195], s[16:17], 0, v[194:195]
	v_lshl_add_u64 v[194:195], s[68:69], 3, v[194:195]
	v_pk_add_f32 v[200:201], v[202:203], v[198:199]
	global_store_dwordx2 v[194:195], v[200:201], off
	s_or_b64 exec, exec, s[4:5]
.Lg9_nostat_2:
	v_add_u32_e32 v192, 0x30, v148
	v_ashrrev_i32_e32 v193, 31, v192
	v_lshlrev_b64 v[194:195], 12, v[192:193]
	v_lshl_add_u64 v[196:197], v[146:147], 0, v[194:195]
	v_pk_add_f32 v[92:93], v[92:93], v[204:205]
	v_pk_add_f32 v[94:95], v[94:95], v[206:207]
	v_pk_add_f32 v[88:89], v[88:89], v[208:209]
	v_pk_add_f32 v[90:91], v[90:91], v[210:211]
	v_med3_f32 v160, v92, s78, v158
	v_med3_f32 v161, v93, s78, v158
	v_med3_f32 v162, v94, s78, v158
	v_med3_f32 v163, v95, s78, v158
	v_med3_f32 v164, v88, s78, v158
	v_med3_f32 v165, v89, s78, v158
	v_med3_f32 v166, v90, s78, v158
	v_med3_f32 v167, v91, s78, v158
	v_pk_mul_f32 v[168:169], v[160:161], v[160:161]
	v_pk_mul_f32 v[170:171], v[162:163], v[162:163]
	v_pk_mul_f32 v[172:173], v[164:165], v[164:165]
	v_pk_mul_f32 v[174:175], v[166:167], v[166:167]
	v_pk_fma_f32 v[168:169], v[168:169], s[20:21], -1.0 op_sel_hi:[1,0,0]
	v_pk_fma_f32 v[170:171], v[170:171], s[20:21], -1.0 op_sel_hi:[1,0,0]
	v_pk_fma_f32 v[172:173], v[172:173], s[20:21], -1.0 op_sel_hi:[1,0,0]
	v_pk_fma_f32 v[174:175], v[174:175], s[20:21], -1.0 op_sel_hi:[1,0,0]
	v_pk_fma_f32 v[176:177], v[168:169], s[22:23], v[150:151] op_sel_hi:[1,0,0] neg_lo:[1,0,0] neg_hi:[1,0,0]
	v_pk_fma_f32 v[178:179], v[170:171], s[22:23], v[150:151] op_sel_hi:[1,0,0] neg_lo:[1,0,0] neg_hi:[1,0,0]
	v_pk_fma_f32 v[180:181], v[172:173], s[22:23], v[150:151] op_sel_hi:[1,0,0] neg_lo:[1,0,0] neg_hi:[1,0,0]
	v_pk_fma_f32 v[182:183], v[174:175], s[22:23], v[150:151] op_sel_hi:[1,0,0] neg_lo:[1,0,0] neg_hi:[1,0,0]
	v_pk_fma_f32 v[176:177], v[168:169], v[176:177], s[26:27] op_sel_hi:[1,1,0]
	v_pk_fma_f32 v[178:179], v[170:171], v[178:179], s[26:27] op_sel_hi:[1,1,0]
	v_pk_fma_f32 v[180:181], v[172:173], v[180:181], s[26:27] op_sel_hi:[1,1,0]
	v_pk_fma_f32 v[182:183], v[174:175], v[182:183], s[26:27] op_sel_hi:[1,1,0]
	v_pk_fma_f32 v[176:177], v[168:169], v[176:177], s[28:29] op_sel_hi:[1,1,0]
	v_pk_fma_f32 v[178:179], v[170:171], v[178:179], s[28:29] op_sel_hi:[1,1,0]
	v_pk_fma_f32 v[180:181], v[172:173], v[180:181], s[28:29] op_sel_hi:[1,1,0]
	v_pk_fma_f32 v[182:183], v[174:175], v[182:183], s[28:29] op_sel_hi:[1,1,0]
	v_pk_fma_f32 v[176:177], v[168:169], v[176:177], s[30:31] op_sel_hi:[1,1,0]
	v_pk_fma_f32 v[178:179], v[170:171], v[178:179], s[30:31] op_sel_hi:[1,1,0]
	v_pk_fma_f32 v[180:181], v[172:173], v[180:181], s[30:31] op_sel_hi:[1,1,0]
	v_pk_fma_f32 v[182:183], v[174:175], v[182:183], s[30:31] op_sel_hi:[1,1,0]
	v_pk_fma_f32 v[176:177], v[168:169], v[176:177], s[34:35] op_sel_hi:[1,1,0]
	v_pk_fma_f32 v[178:179], v[170:171], v[178:179], s[34:35] op_sel_hi:[1,1,0]
	v_pk_fma_f32 v[180:181], v[172:173], v[180:181], s[34:35] op_sel_hi:[1,1,0]
	v_pk_fma_f32 v[182:183], v[174:175], v[182:183], s[34:35] op_sel_hi:[1,1,0]
	v_pk_fma_f32 v[176:177], v[168:169], v[176:177], s[36:37] op_sel_hi:[1,1,0]
	v_pk_fma_f32 v[178:179], v[170:171], v[178:179], s[36:37] op_sel_hi:[1,1,0]
	v_pk_fma_f32 v[180:181], v[172:173], v[180:181], s[36:37] op_sel_hi:[1,1,0]
	v_pk_fma_f32 v[182:183], v[174:175], v[182:183], s[36:37] op_sel_hi:[1,1,0]
	v_pk_fma_f32 v[176:177], v[168:169], v[176:177], s[38:39] op_sel_hi:[1,1,0]
	v_pk_fma_f32 v[178:179], v[170:171], v[178:179], s[38:39] op_sel_hi:[1,1,0]
	v_pk_fma_f32 v[180:181], v[172:173], v[180:181], s[38:39] op_sel_hi:[1,1,0]
	v_pk_fma_f32 v[182:183], v[174:175], v[182:183], s[38:39] op_sel_hi:[1,1,0]
	v_pk_fma_f32 v[176:177], v[168:169], v[176:177], s[40:41] op_sel_hi:[1,1,0]
	v_pk_fma_f32 v[178:179], v[170:171], v[178:179], s[40:41] op_sel_hi:[1,1,0]
	v_pk_fma_f32 v[180:181], v[172:173], v[180:181], s[40:41] op_sel_hi:[1,1,0]
	v_pk_fma_f32 v[182:183], v[174:175], v[182:183], s[40:41] op_sel_hi:[1,1,0]
	v_pk_fma_f32 v[176:177], v[168:169], v[176:177], s[42:43] op_sel_hi:[1,1,0]
	v_pk_fma_f32 v[178:179], v[170:171], v[178:179], s[42:43] op_sel_hi:[1,1,0]
	v_pk_fma_f32 v[180:181], v[172:173], v[180:181], s[42:43] op_sel_hi:[1,1,0]
	v_pk_fma_f32 v[182:183], v[174:175], v[182:183], s[42:43] op_sel_hi:[1,1,0]
	v_pk_fma_f32 v[176:177], v[168:169], v[176:177], s[44:45] op_sel_hi:[1,1,0]
	v_pk_fma_f32 v[178:179], v[170:171], v[178:179], s[44:45] op_sel_hi:[1,1,0]
	v_pk_fma_f32 v[180:181], v[172:173], v[180:181], s[44:45] op_sel_hi:[1,1,0]
	v_pk_fma_f32 v[182:183], v[174:175], v[182:183], s[44:45] op_sel_hi:[1,1,0]
	v_pk_fma_f32 v[168:169], v[168:169], v[176:177], s[48:49] op_sel_hi:[1,1,0]
	v_pk_fma_f32 v[170:171], v[170:171], v[178:179], s[48:49] op_sel_hi:[1,1,0]
	v_pk_fma_f32 v[172:173], v[172:173], v[180:181], s[48:49] op_sel_hi:[1,1,0]
	v_pk_fma_f32 v[174:175], v[174:175], v[182:183], s[48:49] op_sel_hi:[1,1,0]
	v_pk_fma_f32 v[160:161], v[160:161], v[168:169], 0.5 op_sel_hi:[1,1,0]
	v_pk_fma_f32 v[162:163], v[162:163], v[170:171], 0.5 op_sel_hi:[1,1,0]
	v_pk_fma_f32 v[164:165], v[164:165], v[172:173], 0.5 op_sel_hi:[1,1,0]
	v_pk_fma_f32 v[166:167], v[166:167], v[174:175], 0.5 op_sel_hi:[1,1,0]
	v_pk_mul_f32 v[92:93], v[92:93], v[160:161]
	v_pk_mul_f32 v[94:95], v[94:95], v[162:163]
	v_pk_mul_f32 v[88:89], v[88:89], v[164:165]
	v_pk_mul_f32 v[90:91], v[90:91], v[166:167]
	v_cvt_pk_bf16_f32 v184, v92, v93
	v_cvt_pk_bf16_f32 v185, v94, v95
	v_cvt_pk_bf16_f32 v186, v88, v89
	v_cvt_pk_bf16_f32 v187, v90, v91
	global_store_dwordx4 v[196:197], v[184:187], off
	v_pk_add_f32 v[84:85], v[84:85], v[212:213]
	v_pk_add_f32 v[86:87], v[86:87], v[214:215]
	v_pk_add_f32 v[80:81], v[80:81], v[216:217]
	v_pk_add_f32 v[82:83], v[82:83], v[218:219]
	v_med3_f32 v160, v84, s78, v158
	v_med3_f32 v161, v85, s78, v158
	v_med3_f32 v162, v86, s78, v158
	v_med3_f32 v163, v87, s78, v158
	v_med3_f32 v164, v80, s78, v158
	v_med3_f32 v165, v81, s78, v158
	v_med3_f32 v166, v82, s78, v158
	v_med3_f32 v167, v83, s78, v158
	v_pk_mul_f32 v[168:169], v[160:161], v[160:161]
	v_pk_mul_f32 v[170:171], v[162:163], v[162:163]
	v_pk_mul_f32 v[172:173], v[164:165], v[164:165]
	v_pk_mul_f32 v[174:175], v[166:167], v[166:167]
	v_pk_fma_f32 v[168:169], v[168:169], s[20:21], -1.0 op_sel_hi:[1,0,0]
	v_pk_fma_f32 v[170:171], v[170:171], s[20:21], -1.0 op_sel_hi:[1,0,0]
	v_pk_fma_f32 v[172:173], v[172:173], s[20:21], -1.0 op_sel_hi:[1,0,0]
	v_pk_fma_f32 v[174:175], v[174:175], s[20:21], -1.0 op_sel_hi:[1,0,0]
	v_pk_fma_f32 v[176:177], v[168:169], s[22:23], v[150:151] op_sel_hi:[1,0,0] neg_lo:[1,0,0] neg_hi:[1,0,0]
	v_pk_fma_f32 v[178:179], v[170:171], s[22:23], v[150:151] op_sel_hi:[1,0,0] neg_lo:[1,0,0] neg_hi:[1,0,0]
	v_pk_fma_f32 v[180:181], v[172:173], s[22:23], v[150:151] op_sel_hi:[1,0,0] neg_lo:[1,0,0] neg_hi:[1,0,0]
	v_pk_fma_f32 v[182:183], v[174:175], s[22:23], v[150:151] op_sel_hi:[1,0,0] neg_lo:[1,0,0] neg_hi:[1,0,0]
	v_pk_fma_f32 v[176:177], v[168:169], v[176:177], s[26:27] op_sel_hi:[1,1,0]
	v_pk_fma_f32 v[178:179], v[170:171], v[178:179], s[26:27] op_sel_hi:[1,1,0]
	v_pk_fma_f32 v[180:181], v[172:173], v[180:181], s[26:27] op_sel_hi:[1,1,0]
	v_pk_fma_f32 v[182:183], v[174:175], v[182:183], s[26:27] op_sel_hi:[1,1,0]
	v_pk_fma_f32 v[176:177], v[168:169], v[176:177], s[28:29] op_sel_hi:[1,1,0]
	v_pk_fma_f32 v[178:179], v[170:171], v[178:179], s[28:29] op_sel_hi:[1,1,0]
	v_pk_fma_f32 v[180:181], v[172:173], v[180:181], s[28:29] op_sel_hi:[1,1,0]
	v_pk_fma_f32 v[182:183], v[174:175], v[182:183], s[28:29] op_sel_hi:[1,1,0]
	v_pk_fma_f32 v[176:177], v[168:169], v[176:177], s[30:31] op_sel_hi:[1,1,0]
	v_pk_fma_f32 v[178:179], v[170:171], v[178:179], s[30:31] op_sel_hi:[1,1,0]
	v_pk_fma_f32 v[180:181], v[172:173], v[180:181], s[30:31] op_sel_hi:[1,1,0]
	v_pk_fma_f32 v[182:183], v[174:175], v[182:183], s[30:31] op_sel_hi:[1,1,0]
	v_pk_fma_f32 v[176:177], v[168:169], v[176:177], s[34:35] op_sel_hi:[1,1,0]
	v_pk_fma_f32 v[178:179], v[170:171], v[178:179], s[34:35] op_sel_hi:[1,1,0]
	v_pk_fma_f32 v[180:181], v[172:173], v[180:181], s[34:35] op_sel_hi:[1,1,0]
	v_pk_fma_f32 v[182:183], v[174:175], v[182:183], s[34:35] op_sel_hi:[1,1,0]
	v_pk_fma_f32 v[176:177], v[168:169], v[176:177], s[36:37] op_sel_hi:[1,1,0]
	v_pk_fma_f32 v[178:179], v[170:171], v[178:179], s[36:37] op_sel_hi:[1,1,0]
	v_pk_fma_f32 v[180:181], v[172:173], v[180:181], s[36:37] op_sel_hi:[1,1,0]
	v_pk_fma_f32 v[182:183], v[174:175], v[182:183], s[36:37] op_sel_hi:[1,1,0]
	v_pk_fma_f32 v[176:177], v[168:169], v[176:177], s[38:39] op_sel_hi:[1,1,0]
	v_pk_fma_f32 v[178:179], v[170:171], v[178:179], s[38:39] op_sel_hi:[1,1,0]
	v_pk_fma_f32 v[180:181], v[172:173], v[180:181], s[38:39] op_sel_hi:[1,1,0]
	v_pk_fma_f32 v[182:183], v[174:175], v[182:183], s[38:39] op_sel_hi:[1,1,0]
	v_pk_fma_f32 v[176:177], v[168:169], v[176:177], s[40:41] op_sel_hi:[1,1,0]
	v_pk_fma_f32 v[178:179], v[170:171], v[178:179], s[40:41] op_sel_hi:[1,1,0]
	v_pk_fma_f32 v[180:181], v[172:173], v[180:181], s[40:41] op_sel_hi:[1,1,0]
	v_pk_fma_f32 v[182:183], v[174:175], v[182:183], s[40:41] op_sel_hi:[1,1,0]
	v_pk_fma_f32 v[176:177], v[168:169], v[176:177], s[42:43] op_sel_hi:[1,1,0]
	v_pk_fma_f32 v[178:179], v[170:171], v[178:179], s[42:43] op_sel_hi:[1,1,0]
	v_pk_fma_f32 v[180:181], v[172:173], v[180:181], s[42:43] op_sel_hi:[1,1,0]
	v_pk_fma_f32 v[182:183], v[174:175], v[182:183], s[42:43] op_sel_hi:[1,1,0]
	v_pk_fma_f32 v[176:177], v[168:169], v[176:177], s[44:45] op_sel_hi:[1,1,0]
	v_pk_fma_f32 v[178:179], v[170:171], v[178:179], s[44:45] op_sel_hi:[1,1,0]
	v_pk_fma_f32 v[180:181], v[172:173], v[180:181], s[44:45] op_sel_hi:[1,1,0]
	v_pk_fma_f32 v[182:183], v[174:175], v[182:183], s[44:45] op_sel_hi:[1,1,0]
	v_pk_fma_f32 v[168:169], v[168:169], v[176:177], s[48:49] op_sel_hi:[1,1,0]
	v_pk_fma_f32 v[170:171], v[170:171], v[178:179], s[48:49] op_sel_hi:[1,1,0]
	v_pk_fma_f32 v[172:173], v[172:173], v[180:181], s[48:49] op_sel_hi:[1,1,0]
	v_pk_fma_f32 v[174:175], v[174:175], v[182:183], s[48:49] op_sel_hi:[1,1,0]
	v_pk_fma_f32 v[160:161], v[160:161], v[168:169], 0.5 op_sel_hi:[1,1,0]
	v_pk_fma_f32 v[162:163], v[162:163], v[170:171], 0.5 op_sel_hi:[1,1,0]
	v_pk_fma_f32 v[164:165], v[164:165], v[172:173], 0.5 op_sel_hi:[1,1,0]
	v_pk_fma_f32 v[166:167], v[166:167], v[174:175], 0.5 op_sel_hi:[1,1,0]
	v_pk_mul_f32 v[84:85], v[84:85], v[160:161]
	v_pk_mul_f32 v[86:87], v[86:87], v[162:163]
	v_pk_mul_f32 v[80:81], v[80:81], v[164:165]
	v_pk_mul_f32 v[82:83], v[82:83], v[166:167]
	v_cvt_pk_bf16_f32 v188, v84, v85
	v_cvt_pk_bf16_f32 v189, v86, v87
	v_cvt_pk_bf16_f32 v190, v80, v81
	v_cvt_pk_bf16_f32 v191, v82, v83
	global_store_dwordx4 v[196:197], v[188:191], off offset:256
	s_and_b64 vcc, exec, s[70:71]
	s_cbranch_vccz .Lg9_nostat_3
	v_pk_add_f32 v[160:161], v[92:93], v[94:95]
	v_pk_add_f32 v[162:163], v[88:89], v[90:91]
	v_pk_add_f32 v[164:165], v[84:85], v[86:87]
	v_pk_add_f32 v[166:167], v[80:81], v[82:83]
	v_pk_mul_f32 v[168:169], v[92:93], v[92:93]
	v_pk_mul_f32 v[170:171], v[84:85], v[84:85]
	v_pk_add_f32 v[160:161], v[160:161], v[162:163]
	v_pk_add_f32 v[164:165], v[164:165], v[166:167]
	v_pk_fma_f32 v[168:169], v[94:95], v[94:95], v[168:169]
	v_pk_fma_f32 v[170:171], v[86:87], v[86:87], v[170:171]
	v_pk_fma_f32 v[168:169], v[88:89], v[88:89], v[168:169]
	v_pk_fma_f32 v[170:171], v[80:81], v[80:81], v[170:171]
	v_pk_fma_f32 v[168:169], v[90:91], v[90:91], v[168:169]
	v_pk_fma_f32 v[170:171], v[82:83], v[82:83], v[170:171]
	v_pk_add_f32 v[160:161], v[160:161], v[164:165]
	v_pk_add_f32 v[168:169], v[168:169], v[170:171]
	s_nop 0
	v_add_f32_e32 v198, v160, v161
	v_add_f32_e32 v200, v168, v169
	v_mov_b32_e32 v199, v198
	s_nop 1
	v_permlane16_swap_b32 v199, v198
	s_nop 1
	v_add_f32_e32 v198, v199, v198
	v_mov_b32_e32 v202, v198
	v_mov_b32_e32 v201, v200
	s_nop 1
	v_permlane32_swap_b32 v202, v198
	s_nop 1
	s_nop 1
	v_permlane16_swap_b32 v201, v200
	s_nop 1
	v_add_f32_e32 v199, v201, v200
	v_mov_b32_e32 v203, v199
	s_nop 1
	v_permlane32_swap_b32 v203, v199
	s_nop 1
	s_and_saveexec_b64 s[4:5], s[6:7]
	v_lshlrev_b64 v[194:195], 8, v[192:193]
	v_lshl_add_u64 v[194:195], s[16:17], 0, v[194:195]
	v_lshl_add_u64 v[194:195], s[68:69], 3, v[194:195]
	v_pk_add_f32 v[200:201], v[202:203], v[198:199]
	global_store_dwordx2 v[194:195], v[200:201], off
	s_or_b64 exec, exec, s[4:5]
.Lg9_nostat_3:
	v_add_u32_e32 v192, 0x80, v148
	v_ashrrev_i32_e32 v193, 31, v192
	v_lshlrev_b64 v[194:195], 12, v[192:193]
	v_lshl_add_u64 v[196:197], v[146:147], 0, v[194:195]
	v_pk_add_f32 v[72:73], v[72:73], v[204:205]
	v_pk_add_f32 v[74:75], v[74:75], v[206:207]
	v_pk_add_f32 v[64:65], v[64:65], v[208:209]
	v_pk_add_f32 v[66:67], v[66:67], v[210:211]
	v_med3_f32 v160, v72, s78, v158
	v_med3_f32 v161, v73, s78, v158
	v_med3_f32 v162, v74, s78, v158
	v_med3_f32 v163, v75, s78, v158
	v_med3_f32 v164, v64, s78, v158
	v_med3_f32 v165, v65, s78, v158
	v_med3_f32 v166, v66, s78, v158
	v_med3_f32 v167, v67, s78, v158
	v_pk_mul_f32 v[168:169], v[160:161], v[160:161]
	v_pk_mul_f32 v[170:171], v[162:163], v[162:163]
	v_pk_mul_f32 v[172:173], v[164:165], v[164:165]
	v_pk_mul_f32 v[174:175], v[166:167], v[166:167]
	v_pk_fma_f32 v[168:169], v[168:169], s[20:21], -1.0 op_sel_hi:[1,0,0]
	v_pk_fma_f32 v[170:171], v[170:171], s[20:21], -1.0 op_sel_hi:[1,0,0]
	v_pk_fma_f32 v[172:173], v[172:173], s[20:21], -1.0 op_sel_hi:[1,0,0]
	v_pk_fma_f32 v[174:175], v[174:175], s[20:21], -1.0 op_sel_hi:[1,0,0]
	v_pk_fma_f32 v[176:177], v[168:169], s[22:23], v[150:151] op_sel_hi:[1,0,0] neg_lo:[1,0,0] neg_hi:[1,0,0]
	v_pk_fma_f32 v[178:179], v[170:171], s[22:23], v[150:151] op_sel_hi:[1,0,0] neg_lo:[1,0,0] neg_hi:[1,0,0]
	v_pk_fma_f32 v[180:181], v[172:173], s[22:23], v[150:151] op_sel_hi:[1,0,0] neg_lo:[1,0,0] neg_hi:[1,0,0]
	v_pk_fma_f32 v[182:183], v[174:175], s[22:23], v[150:151] op_sel_hi:[1,0,0] neg_lo:[1,0,0] neg_hi:[1,0,0]
	v_pk_fma_f32 v[176:177], v[168:169], v[176:177], s[26:27] op_sel_hi:[1,1,0]
	v_pk_fma_f32 v[178:179], v[170:171], v[178:179], s[26:27] op_sel_hi:[1,1,0]
	v_pk_fma_f32 v[180:181], v[172:173], v[180:181], s[26:27] op_sel_hi:[1,1,0]
	v_pk_fma_f32 v[182:183], v[174:175], v[182:183], s[26:27] op_sel_hi:[1,1,0]
	v_pk_fma_f32 v[176:177], v[168:169], v[176:177], s[28:29] op_sel_hi:[1,1,0]
	v_pk_fma_f32 v[178:179], v[170:171], v[178:179], s[28:29] op_sel_hi:[1,1,0]
	v_pk_fma_f32 v[180:181], v[172:173], v[180:181], s[28:29] op_sel_hi:[1,1,0]
	v_pk_fma_f32 v[182:183], v[174:175], v[182:183], s[28:29] op_sel_hi:[1,1,0]
	v_pk_fma_f32 v[176:177], v[168:169], v[176:177], s[30:31] op_sel_hi:[1,1,0]
	v_pk_fma_f32 v[178:179], v[170:171], v[178:179], s[30:31] op_sel_hi:[1,1,0]
	v_pk_fma_f32 v[180:181], v[172:173], v[180:181], s[30:31] op_sel_hi:[1,1,0]
	v_pk_fma_f32 v[182:183], v[174:175], v[182:183], s[30:31] op_sel_hi:[1,1,0]
	v_pk_fma_f32 v[176:177], v[168:169], v[176:177], s[34:35] op_sel_hi:[1,1,0]
	v_pk_fma_f32 v[178:179], v[170:171], v[178:179], s[34:35] op_sel_hi:[1,1,0]
	v_pk_fma_f32 v[180:181], v[172:173], v[180:181], s[34:35] op_sel_hi:[1,1,0]
	v_pk_fma_f32 v[182:183], v[174:175], v[182:183], s[34:35] op_sel_hi:[1,1,0]
	v_pk_fma_f32 v[176:177], v[168:169], v[176:177], s[36:37] op_sel_hi:[1,1,0]
	v_pk_fma_f32 v[178:179], v[170:171], v[178:179], s[36:37] op_sel_hi:[1,1,0]
	v_pk_fma_f32 v[180:181], v[172:173], v[180:181], s[36:37] op_sel_hi:[1,1,0]
	v_pk_fma_f32 v[182:183], v[174:175], v[182:183], s[36:37] op_sel_hi:[1,1,0]
	v_pk_fma_f32 v[176:177], v[168:169], v[176:177], s[38:39] op_sel_hi:[1,1,0]
	v_pk_fma_f32 v[178:179], v[170:171], v[178:179], s[38:39] op_sel_hi:[1,1,0]
	v_pk_fma_f32 v[180:181], v[172:173], v[180:181], s[38:39] op_sel_hi:[1,1,0]
	v_pk_fma_f32 v[182:183], v[174:175], v[182:183], s[38:39] op_sel_hi:[1,1,0]
	v_pk_fma_f32 v[176:177], v[168:169], v[176:177], s[40:41] op_sel_hi:[1,1,0]
	v_pk_fma_f32 v[178:179], v[170:171], v[178:179], s[40:41] op_sel_hi:[1,1,0]
	v_pk_fma_f32 v[180:181], v[172:173], v[180:181], s[40:41] op_sel_hi:[1,1,0]
	v_pk_fma_f32 v[182:183], v[174:175], v[182:183], s[40:41] op_sel_hi:[1,1,0]
	v_pk_fma_f32 v[176:177], v[168:169], v[176:177], s[42:43] op_sel_hi:[1,1,0]
	v_pk_fma_f32 v[178:179], v[170:171], v[178:179], s[42:43] op_sel_hi:[1,1,0]
	v_pk_fma_f32 v[180:181], v[172:173], v[180:181], s[42:43] op_sel_hi:[1,1,0]
	v_pk_fma_f32 v[182:183], v[174:175], v[182:183], s[42:43] op_sel_hi:[1,1,0]
	v_pk_fma_f32 v[176:177], v[168:169], v[176:177], s[44:45] op_sel_hi:[1,1,0]
	v_pk_fma_f32 v[178:179], v[170:171], v[178:179], s[44:45] op_sel_hi:[1,1,0]
	v_pk_fma_f32 v[180:181], v[172:173], v[180:181], s[44:45] op_sel_hi:[1,1,0]
	v_pk_fma_f32 v[182:183], v[174:175], v[182:183], s[44:45] op_sel_hi:[1,1,0]
	v_pk_fma_f32 v[168:169], v[168:169], v[176:177], s[48:49] op_sel_hi:[1,1,0]
	v_pk_fma_f32 v[170:171], v[170:171], v[178:179], s[48:49] op_sel_hi:[1,1,0]
	v_pk_fma_f32 v[172:173], v[172:173], v[180:181], s[48:49] op_sel_hi:[1,1,0]
	v_pk_fma_f32 v[174:175], v[174:175], v[182:183], s[48:49] op_sel_hi:[1,1,0]
	v_pk_fma_f32 v[160:161], v[160:161], v[168:169], 0.5 op_sel_hi:[1,1,0]
	v_pk_fma_f32 v[162:163], v[162:163], v[170:171], 0.5 op_sel_hi:[1,1,0]
	v_pk_fma_f32 v[164:165], v[164:165], v[172:173], 0.5 op_sel_hi:[1,1,0]
	v_pk_fma_f32 v[166:167], v[166:167], v[174:175], 0.5 op_sel_hi:[1,1,0]
	v_pk_mul_f32 v[72:73], v[72:73], v[160:161]
	v_pk_mul_f32 v[74:75], v[74:75], v[162:163]
	v_pk_mul_f32 v[64:65], v[64:65], v[164:165]
	v_pk_mul_f32 v[66:67], v[66:67], v[166:167]
	v_cvt_pk_bf16_f32 v184, v72, v73
	v_cvt_pk_bf16_f32 v185, v74, v75
	v_cvt_pk_bf16_f32 v186, v64, v65
	v_cvt_pk_bf16_f32 v187, v66, v67
	global_store_dwordx4 v[196:197], v[184:187], off
	v_pk_add_f32 v[52:53], v[52:53], v[212:213]
	v_pk_add_f32 v[54:55], v[54:55], v[214:215]
	v_pk_add_f32 v[48:49], v[48:49], v[216:217]
	v_pk_add_f32 v[50:51], v[50:51], v[218:219]
	v_med3_f32 v160, v52, s78, v158
	v_med3_f32 v161, v53, s78, v158
	v_med3_f32 v162, v54, s78, v158
	v_med3_f32 v163, v55, s78, v158
	v_med3_f32 v164, v48, s78, v158
	v_med3_f32 v165, v49, s78, v158
	v_med3_f32 v166, v50, s78, v158
	v_med3_f32 v167, v51, s78, v158
	v_pk_mul_f32 v[168:169], v[160:161], v[160:161]
	v_pk_mul_f32 v[170:171], v[162:163], v[162:163]
	v_pk_mul_f32 v[172:173], v[164:165], v[164:165]
	v_pk_mul_f32 v[174:175], v[166:167], v[166:167]
	v_pk_fma_f32 v[168:169], v[168:169], s[20:21], -1.0 op_sel_hi:[1,0,0]
	v_pk_fma_f32 v[170:171], v[170:171], s[20:21], -1.0 op_sel_hi:[1,0,0]
	v_pk_fma_f32 v[172:173], v[172:173], s[20:21], -1.0 op_sel_hi:[1,0,0]
	v_pk_fma_f32 v[174:175], v[174:175], s[20:21], -1.0 op_sel_hi:[1,0,0]
	v_pk_fma_f32 v[176:177], v[168:169], s[22:23], v[150:151] op_sel_hi:[1,0,0] neg_lo:[1,0,0] neg_hi:[1,0,0]
	v_pk_fma_f32 v[178:179], v[170:171], s[22:23], v[150:151] op_sel_hi:[1,0,0] neg_lo:[1,0,0] neg_hi:[1,0,0]
	v_pk_fma_f32 v[180:181], v[172:173], s[22:23], v[150:151] op_sel_hi:[1,0,0] neg_lo:[1,0,0] neg_hi:[1,0,0]
	v_pk_fma_f32 v[182:183], v[174:175], s[22:23], v[150:151] op_sel_hi:[1,0,0] neg_lo:[1,0,0] neg_hi:[1,0,0]
	v_pk_fma_f32 v[176:177], v[168:169], v[176:177], s[26:27] op_sel_hi:[1,1,0]
	v_pk_fma_f32 v[178:179], v[170:171], v[178:179], s[26:27] op_sel_hi:[1,1,0]
	v_pk_fma_f32 v[180:181], v[172:173], v[180:181], s[26:27] op_sel_hi:[1,1,0]
	v_pk_fma_f32 v[182:183], v[174:175], v[182:183], s[26:27] op_sel_hi:[1,1,0]
	v_pk_fma_f32 v[176:177], v[168:169], v[176:177], s[28:29] op_sel_hi:[1,1,0]
	v_pk_fma_f32 v[178:179], v[170:171], v[178:179], s[28:29] op_sel_hi:[1,1,0]
	v_pk_fma_f32 v[180:181], v[172:173], v[180:181], s[28:29] op_sel_hi:[1,1,0]
	v_pk_fma_f32 v[182:183], v[174:175], v[182:183], s[28:29] op_sel_hi:[1,1,0]
	v_pk_fma_f32 v[176:177], v[168:169], v[176:177], s[30:31] op_sel_hi:[1,1,0]
	v_pk_fma_f32 v[178:179], v[170:171], v[178:179], s[30:31] op_sel_hi:[1,1,0]
	v_pk_fma_f32 v[180:181], v[172:173], v[180:181], s[30:31] op_sel_hi:[1,1,0]
	v_pk_fma_f32 v[182:183], v[174:175], v[182:183], s[30:31] op_sel_hi:[1,1,0]
	v_pk_fma_f32 v[176:177], v[168:169], v[176:177], s[34:35] op_sel_hi:[1,1,0]
	v_pk_fma_f32 v[178:179], v[170:171], v[178:179], s[34:35] op_sel_hi:[1,1,0]
	v_pk_fma_f32 v[180:181], v[172:173], v[180:181], s[34:35] op_sel_hi:[1,1,0]
	v_pk_fma_f32 v[182:183], v[174:175], v[182:183], s[34:35] op_sel_hi:[1,1,0]
	v_pk_fma_f32 v[176:177], v[168:169], v[176:177], s[36:37] op_sel_hi:[1,1,0]
	v_pk_fma_f32 v[178:179], v[170:171], v[178:179], s[36:37] op_sel_hi:[1,1,0]
	v_pk_fma_f32 v[180:181], v[172:173], v[180:181], s[36:37] op_sel_hi:[1,1,0]
	v_pk_fma_f32 v[182:183], v[174:175], v[182:183], s[36:37] op_sel_hi:[1,1,0]
	v_pk_fma_f32 v[176:177], v[168:169], v[176:177], s[38:39] op_sel_hi:[1,1,0]
	v_pk_fma_f32 v[178:179], v[170:171], v[178:179], s[38:39] op_sel_hi:[1,1,0]
	v_pk_fma_f32 v[180:181], v[172:173], v[180:181], s[38:39] op_sel_hi:[1,1,0]
	v_pk_fma_f32 v[182:183], v[174:175], v[182:183], s[38:39] op_sel_hi:[1,1,0]
	v_pk_fma_f32 v[176:177], v[168:169], v[176:177], s[40:41] op_sel_hi:[1,1,0]
	v_pk_fma_f32 v[178:179], v[170:171], v[178:179], s[40:41] op_sel_hi:[1,1,0]
	v_pk_fma_f32 v[180:181], v[172:173], v[180:181], s[40:41] op_sel_hi:[1,1,0]
	v_pk_fma_f32 v[182:183], v[174:175], v[182:183], s[40:41] op_sel_hi:[1,1,0]
	v_pk_fma_f32 v[176:177], v[168:169], v[176:177], s[42:43] op_sel_hi:[1,1,0]
	v_pk_fma_f32 v[178:179], v[170:171], v[178:179], s[42:43] op_sel_hi:[1,1,0]
	v_pk_fma_f32 v[180:181], v[172:173], v[180:181], s[42:43] op_sel_hi:[1,1,0]
	v_pk_fma_f32 v[182:183], v[174:175], v[182:183], s[42:43] op_sel_hi:[1,1,0]
	v_pk_fma_f32 v[176:177], v[168:169], v[176:177], s[44:45] op_sel_hi:[1,1,0]
	v_pk_fma_f32 v[178:179], v[170:171], v[178:179], s[44:45] op_sel_hi:[1,1,0]
	v_pk_fma_f32 v[180:181], v[172:173], v[180:181], s[44:45] op_sel_hi:[1,1,0]
	v_pk_fma_f32 v[182:183], v[174:175], v[182:183], s[44:45] op_sel_hi:[1,1,0]
	v_pk_fma_f32 v[168:169], v[168:169], v[176:177], s[48:49] op_sel_hi:[1,1,0]
	v_pk_fma_f32 v[170:171], v[170:171], v[178:179], s[48:49] op_sel_hi:[1,1,0]
	v_pk_fma_f32 v[172:173], v[172:173], v[180:181], s[48:49] op_sel_hi:[1,1,0]
	v_pk_fma_f32 v[174:175], v[174:175], v[182:183], s[48:49] op_sel_hi:[1,1,0]
	v_pk_fma_f32 v[160:161], v[160:161], v[168:169], 0.5 op_sel_hi:[1,1,0]
	v_pk_fma_f32 v[162:163], v[162:163], v[170:171], 0.5 op_sel_hi:[1,1,0]
	v_pk_fma_f32 v[164:165], v[164:165], v[172:173], 0.5 op_sel_hi:[1,1,0]
	v_pk_fma_f32 v[166:167], v[166:167], v[174:175], 0.5 op_sel_hi:[1,1,0]
	v_pk_mul_f32 v[52:53], v[52:53], v[160:161]
	v_pk_mul_f32 v[54:55], v[54:55], v[162:163]
	v_pk_mul_f32 v[48:49], v[48:49], v[164:165]
	v_pk_mul_f32 v[50:51], v[50:51], v[166:167]
	v_cvt_pk_bf16_f32 v188, v52, v53
	v_cvt_pk_bf16_f32 v189, v54, v55
	v_cvt_pk_bf16_f32 v190, v48, v49
	v_cvt_pk_bf16_f32 v191, v50, v51
	global_store_dwordx4 v[196:197], v[188:191], off offset:256
	s_and_b64 vcc, exec, s[70:71]
	s_cbranch_vccz .Lg9_nostat_4
	v_pk_add_f32 v[160:161], v[72:73], v[74:75]
	v_pk_add_f32 v[162:163], v[64:65], v[66:67]
	v_pk_add_f32 v[164:165], v[52:53], v[54:55]
	v_pk_add_f32 v[166:167], v[48:49], v[50:51]
	v_pk_mul_f32 v[168:169], v[72:73], v[72:73]
	v_pk_mul_f32 v[170:171], v[52:53], v[52:53]
	v_pk_add_f32 v[160:161], v[160:161], v[162:163]
	v_pk_add_f32 v[164:165], v[164:165], v[166:167]
	v_pk_fma_f32 v[168:169], v[74:75], v[74:75], v[168:169]
	v_pk_fma_f32 v[170:171], v[54:55], v[54:55], v[170:171]
	v_pk_fma_f32 v[168:169], v[64:65], v[64:65], v[168:169]
	v_pk_fma_f32 v[170:171], v[48:49], v[48:49], v[170:171]
	v_pk_fma_f32 v[168:169], v[66:67], v[66:67], v[168:169]
	v_pk_fma_f32 v[170:171], v[50:51], v[50:51], v[170:171]
	v_pk_add_f32 v[160:161], v[160:161], v[164:165]
	v_pk_add_f32 v[168:169], v[168:169], v[170:171]
	s_nop 0
	v_add_f32_e32 v198, v160, v161
	v_add_f32_e32 v200, v168, v169
	v_mov_b32_e32 v199, v198
	s_nop 1
	v_permlane16_swap_b32 v199, v198
	s_nop 1
	v_add_f32_e32 v198, v199, v198
	v_mov_b32_e32 v202, v198
	v_mov_b32_e32 v201, v200
	s_nop 1
	v_permlane32_swap_b32 v202, v198
	s_nop 1
	s_nop 1
	v_permlane16_swap_b32 v201, v200
	s_nop 1
	v_add_f32_e32 v199, v201, v200
	v_mov_b32_e32 v203, v199
	s_nop 1
	v_permlane32_swap_b32 v203, v199
	s_nop 1
	s_and_saveexec_b64 s[4:5], s[6:7]
	v_lshlrev_b64 v[194:195], 8, v[192:193]
	v_lshl_add_u64 v[194:195], s[16:17], 0, v[194:195]
	v_lshl_add_u64 v[194:195], s[68:69], 3, v[194:195]
	v_pk_add_f32 v[200:201], v[202:203], v[198:199]
	global_store_dwordx2 v[194:195], v[200:201], off
	s_or_b64 exec, exec, s[4:5]
.Lg9_nostat_4:
	v_add_u32_e32 v192, 0x90, v148
	v_ashrrev_i32_e32 v193, 31, v192
	v_lshlrev_b64 v[194:195], 12, v[192:193]
	v_lshl_add_u64 v[196:197], v[146:147], 0, v[194:195]
	v_pk_add_f32 v[44:45], v[44:45], v[204:205]
	v_pk_add_f32 v[46:47], v[46:47], v[206:207]
	v_pk_add_f32 v[40:41], v[40:41], v[208:209]
	v_pk_add_f32 v[42:43], v[42:43], v[210:211]
	v_med3_f32 v160, v44, s78, v158
	v_med3_f32 v161, v45, s78, v158
	v_med3_f32 v162, v46, s78, v158
	v_med3_f32 v163, v47, s78, v158
	v_med3_f32 v164, v40, s78, v158
	v_med3_f32 v165, v41, s78, v158
	v_med3_f32 v166, v42, s78, v158
	v_med3_f32 v167, v43, s78, v158
	v_pk_mul_f32 v[168:169], v[160:161], v[160:161]
	v_pk_mul_f32 v[170:171], v[162:163], v[162:163]
	v_pk_mul_f32 v[172:173], v[164:165], v[164:165]
	v_pk_mul_f32 v[174:175], v[166:167], v[166:167]
	v_pk_fma_f32 v[168:169], v[168:169], s[20:21], -1.0 op_sel_hi:[1,0,0]
	v_pk_fma_f32 v[170:171], v[170:171], s[20:21], -1.0 op_sel_hi:[1,0,0]
	v_pk_fma_f32 v[172:173], v[172:173], s[20:21], -1.0 op_sel_hi:[1,0,0]
	v_pk_fma_f32 v[174:175], v[174:175], s[20:21], -1.0 op_sel_hi:[1,0,0]
	v_pk_fma_f32 v[176:177], v[168:169], s[22:23], v[150:151] op_sel_hi:[1,0,0] neg_lo:[1,0,0] neg_hi:[1,0,0]
	v_pk_fma_f32 v[178:179], v[170:171], s[22:23], v[150:151] op_sel_hi:[1,0,0] neg_lo:[1,0,0] neg_hi:[1,0,0]
	v_pk_fma_f32 v[180:181], v[172:173], s[22:23], v[150:151] op_sel_hi:[1,0,0] neg_lo:[1,0,0] neg_hi:[1,0,0]
	v_pk_fma_f32 v[182:183], v[174:175], s[22:23], v[150:151] op_sel_hi:[1,0,0] neg_lo:[1,0,0] neg_hi:[1,0,0]
	v_pk_fma_f32 v[176:177], v[168:169], v[176:177], s[26:27] op_sel_hi:[1,1,0]
	v_pk_fma_f32 v[178:179], v[170:171], v[178:179], s[26:27] op_sel_hi:[1,1,0]
	v_pk_fma_f32 v[180:181], v[172:173], v[180:181], s[26:27] op_sel_hi:[1,1,0]
	v_pk_fma_f32 v[182:183], v[174:175], v[182:183], s[26:27] op_sel_hi:[1,1,0]
	v_pk_fma_f32 v[176:177], v[168:169], v[176:177], s[28:29] op_sel_hi:[1,1,0]
	v_pk_fma_f32 v[178:179], v[170:171], v[178:179], s[28:29] op_sel_hi:[1,1,0]
	v_pk_fma_f32 v[180:181], v[172:173], v[180:181], s[28:29] op_sel_hi:[1,1,0]
	v_pk_fma_f32 v[182:183], v[174:175], v[182:183], s[28:29] op_sel_hi:[1,1,0]
	v_pk_fma_f32 v[176:177], v[168:169], v[176:177], s[30:31] op_sel_hi:[1,1,0]
	v_pk_fma_f32 v[178:179], v[170:171], v[178:179], s[30:31] op_sel_hi:[1,1,0]
	v_pk_fma_f32 v[180:181], v[172:173], v[180:181], s[30:31] op_sel_hi:[1,1,0]
	v_pk_fma_f32 v[182:183], v[174:175], v[182:183], s[30:31] op_sel_hi:[1,1,0]
	v_pk_fma_f32 v[176:177], v[168:169], v[176:177], s[34:35] op_sel_hi:[1,1,0]
	v_pk_fma_f32 v[178:179], v[170:171], v[178:179], s[34:35] op_sel_hi:[1,1,0]
	v_pk_fma_f32 v[180:181], v[172:173], v[180:181], s[34:35] op_sel_hi:[1,1,0]
	v_pk_fma_f32 v[182:183], v[174:175], v[182:183], s[34:35] op_sel_hi:[1,1,0]
	v_pk_fma_f32 v[176:177], v[168:169], v[176:177], s[36:37] op_sel_hi:[1,1,0]
	v_pk_fma_f32 v[178:179], v[170:171], v[178:179], s[36:37] op_sel_hi:[1,1,0]
	v_pk_fma_f32 v[180:181], v[172:173], v[180:181], s[36:37] op_sel_hi:[1,1,0]
	v_pk_fma_f32 v[182:183], v[174:175], v[182:183], s[36:37] op_sel_hi:[1,1,0]
	v_pk_fma_f32 v[176:177], v[168:169], v[176:177], s[38:39] op_sel_hi:[1,1,0]
	v_pk_fma_f32 v[178:179], v[170:171], v[178:179], s[38:39] op_sel_hi:[1,1,0]
	v_pk_fma_f32 v[180:181], v[172:173], v[180:181], s[38:39] op_sel_hi:[1,1,0]
	v_pk_fma_f32 v[182:183], v[174:175], v[182:183], s[38:39] op_sel_hi:[1,1,0]
	v_pk_fma_f32 v[176:177], v[168:169], v[176:177], s[40:41] op_sel_hi:[1,1,0]
	v_pk_fma_f32 v[178:179], v[170:171], v[178:179], s[40:41] op_sel_hi:[1,1,0]
	v_pk_fma_f32 v[180:181], v[172:173], v[180:181], s[40:41] op_sel_hi:[1,1,0]
	v_pk_fma_f32 v[182:183], v[174:175], v[182:183], s[40:41] op_sel_hi:[1,1,0]
	v_pk_fma_f32 v[176:177], v[168:169], v[176:177], s[42:43] op_sel_hi:[1,1,0]
	v_pk_fma_f32 v[178:179], v[170:171], v[178:179], s[42:43] op_sel_hi:[1,1,0]
	v_pk_fma_f32 v[180:181], v[172:173], v[180:181], s[42:43] op_sel_hi:[1,1,0]
	v_pk_fma_f32 v[182:183], v[174:175], v[182:183], s[42:43] op_sel_hi:[1,1,0]
	v_pk_fma_f32 v[176:177], v[168:169], v[176:177], s[44:45] op_sel_hi:[1,1,0]
	v_pk_fma_f32 v[178:179], v[170:171], v[178:179], s[44:45] op_sel_hi:[1,1,0]
	v_pk_fma_f32 v[180:181], v[172:173], v[180:181], s[44:45] op_sel_hi:[1,1,0]
	v_pk_fma_f32 v[182:183], v[174:175], v[182:183], s[44:45] op_sel_hi:[1,1,0]
	v_pk_fma_f32 v[168:169], v[168:169], v[176:177], s[48:49] op_sel_hi:[1,1,0]
	v_pk_fma_f32 v[170:171], v[170:171], v[178:179], s[48:49] op_sel_hi:[1,1,0]
	v_pk_fma_f32 v[172:173], v[172:173], v[180:181], s[48:49] op_sel_hi:[1,1,0]
	v_pk_fma_f32 v[174:175], v[174:175], v[182:183], s[48:49] op_sel_hi:[1,1,0]
	v_pk_fma_f32 v[160:161], v[160:161], v[168:169], 0.5 op_sel_hi:[1,1,0]
	v_pk_fma_f32 v[162:163], v[162:163], v[170:171], 0.5 op_sel_hi:[1,1,0]
	v_pk_fma_f32 v[164:165], v[164:165], v[172:173], 0.5 op_sel_hi:[1,1,0]
	v_pk_fma_f32 v[166:167], v[166:167], v[174:175], 0.5 op_sel_hi:[1,1,0]
	v_pk_mul_f32 v[44:45], v[44:45], v[160:161]
	v_pk_mul_f32 v[46:47], v[46:47], v[162:163]
	v_pk_mul_f32 v[40:41], v[40:41], v[164:165]
	v_pk_mul_f32 v[42:43], v[42:43], v[166:167]
	v_cvt_pk_bf16_f32 v184, v44, v45
	v_cvt_pk_bf16_f32 v185, v46, v47
	v_cvt_pk_bf16_f32 v186, v40, v41
	v_cvt_pk_bf16_f32 v187, v42, v43
	global_store_dwordx4 v[196:197], v[184:187], off
	v_pk_add_f32 v[36:37], v[36:37], v[212:213]
	v_pk_add_f32 v[38:39], v[38:39], v[214:215]
	v_pk_add_f32 v[32:33], v[32:33], v[216:217]
	v_pk_add_f32 v[34:35], v[34:35], v[218:219]
	v_med3_f32 v160, v36, s78, v158
	v_med3_f32 v161, v37, s78, v158
	v_med3_f32 v162, v38, s78, v158
	v_med3_f32 v163, v39, s78, v158
	v_med3_f32 v164, v32, s78, v158
	v_med3_f32 v165, v33, s78, v158
	v_med3_f32 v166, v34, s78, v158
	v_med3_f32 v167, v35, s78, v158
	v_pk_mul_f32 v[168:169], v[160:161], v[160:161]
	v_pk_mul_f32 v[170:171], v[162:163], v[162:163]
	v_pk_mul_f32 v[172:173], v[164:165], v[164:165]
	v_pk_mul_f32 v[174:175], v[166:167], v[166:167]
	v_pk_fma_f32 v[168:169], v[168:169], s[20:21], -1.0 op_sel_hi:[1,0,0]
	v_pk_fma_f32 v[170:171], v[170:171], s[20:21], -1.0 op_sel_hi:[1,0,0]
	v_pk_fma_f32 v[172:173], v[172:173], s[20:21], -1.0 op_sel_hi:[1,0,0]
	v_pk_fma_f32 v[174:175], v[174:175], s[20:21], -1.0 op_sel_hi:[1,0,0]
	v_pk_fma_f32 v[176:177], v[168:169], s[22:23], v[150:151] op_sel_hi:[1,0,0] neg_lo:[1,0,0] neg_hi:[1,0,0]
	v_pk_fma_f32 v[178:179], v[170:171], s[22:23], v[150:151] op_sel_hi:[1,0,0] neg_lo:[1,0,0] neg_hi:[1,0,0]
	v_pk_fma_f32 v[180:181], v[172:173], s[22:23], v[150:151] op_sel_hi:[1,0,0] neg_lo:[1,0,0] neg_hi:[1,0,0]
	v_pk_fma_f32 v[182:183], v[174:175], s[22:23], v[150:151] op_sel_hi:[1,0,0] neg_lo:[1,0,0] neg_hi:[1,0,0]
	v_pk_fma_f32 v[176:177], v[168:169], v[176:177], s[26:27] op_sel_hi:[1,1,0]
	v_pk_fma_f32 v[178:179], v[170:171], v[178:179], s[26:27] op_sel_hi:[1,1,0]
	v_pk_fma_f32 v[180:181], v[172:173], v[180:181], s[26:27] op_sel_hi:[1,1,0]
	v_pk_fma_f32 v[182:183], v[174:175], v[182:183], s[26:27] op_sel_hi:[1,1,0]
	v_pk_fma_f32 v[176:177], v[168:169], v[176:177], s[28:29] op_sel_hi:[1,1,0]
	v_pk_fma_f32 v[178:179], v[170:171], v[178:179], s[28:29] op_sel_hi:[1,1,0]
	v_pk_fma_f32 v[180:181], v[172:173], v[180:181], s[28:29] op_sel_hi:[1,1,0]
	v_pk_fma_f32 v[182:183], v[174:175], v[182:183], s[28:29] op_sel_hi:[1,1,0]
	v_pk_fma_f32 v[176:177], v[168:169], v[176:177], s[30:31] op_sel_hi:[1,1,0]
	v_pk_fma_f32 v[178:179], v[170:171], v[178:179], s[30:31] op_sel_hi:[1,1,0]
	v_pk_fma_f32 v[180:181], v[172:173], v[180:181], s[30:31] op_sel_hi:[1,1,0]
	v_pk_fma_f32 v[182:183], v[174:175], v[182:183], s[30:31] op_sel_hi:[1,1,0]
	v_pk_fma_f32 v[176:177], v[168:169], v[176:177], s[34:35] op_sel_hi:[1,1,0]
	v_pk_fma_f32 v[178:179], v[170:171], v[178:179], s[34:35] op_sel_hi:[1,1,0]
	v_pk_fma_f32 v[180:181], v[172:173], v[180:181], s[34:35] op_sel_hi:[1,1,0]
	v_pk_fma_f32 v[182:183], v[174:175], v[182:183], s[34:35] op_sel_hi:[1,1,0]
	v_pk_fma_f32 v[176:177], v[168:169], v[176:177], s[36:37] op_sel_hi:[1,1,0]
	v_pk_fma_f32 v[178:179], v[170:171], v[178:179], s[36:37] op_sel_hi:[1,1,0]
	v_pk_fma_f32 v[180:181], v[172:173], v[180:181], s[36:37] op_sel_hi:[1,1,0]
	v_pk_fma_f32 v[182:183], v[174:175], v[182:183], s[36:37] op_sel_hi:[1,1,0]
	v_pk_fma_f32 v[176:177], v[168:169], v[176:177], s[38:39] op_sel_hi:[1,1,0]
	v_pk_fma_f32 v[178:179], v[170:171], v[178:179], s[38:39] op_sel_hi:[1,1,0]
	v_pk_fma_f32 v[180:181], v[172:173], v[180:181], s[38:39] op_sel_hi:[1,1,0]
	v_pk_fma_f32 v[182:183], v[174:175], v[182:183], s[38:39] op_sel_hi:[1,1,0]
	v_pk_fma_f32 v[176:177], v[168:169], v[176:177], s[40:41] op_sel_hi:[1,1,0]
	v_pk_fma_f32 v[178:179], v[170:171], v[178:179], s[40:41] op_sel_hi:[1,1,0]
	v_pk_fma_f32 v[180:181], v[172:173], v[180:181], s[40:41] op_sel_hi:[1,1,0]
	v_pk_fma_f32 v[182:183], v[174:175], v[182:183], s[40:41] op_sel_hi:[1,1,0]
	v_pk_fma_f32 v[176:177], v[168:169], v[176:177], s[42:43] op_sel_hi:[1,1,0]
	v_pk_fma_f32 v[178:179], v[170:171], v[178:179], s[42:43] op_sel_hi:[1,1,0]
	v_pk_fma_f32 v[180:181], v[172:173], v[180:181], s[42:43] op_sel_hi:[1,1,0]
	v_pk_fma_f32 v[182:183], v[174:175], v[182:183], s[42:43] op_sel_hi:[1,1,0]
	v_pk_fma_f32 v[176:177], v[168:169], v[176:177], s[44:45] op_sel_hi:[1,1,0]
	v_pk_fma_f32 v[178:179], v[170:171], v[178:179], s[44:45] op_sel_hi:[1,1,0]
	v_pk_fma_f32 v[180:181], v[172:173], v[180:181], s[44:45] op_sel_hi:[1,1,0]
	v_pk_fma_f32 v[182:183], v[174:175], v[182:183], s[44:45] op_sel_hi:[1,1,0]
	v_pk_fma_f32 v[168:169], v[168:169], v[176:177], s[48:49] op_sel_hi:[1,1,0]
	v_pk_fma_f32 v[170:171], v[170:171], v[178:179], s[48:49] op_sel_hi:[1,1,0]
	v_pk_fma_f32 v[172:173], v[172:173], v[180:181], s[48:49] op_sel_hi:[1,1,0]
	v_pk_fma_f32 v[174:175], v[174:175], v[182:183], s[48:49] op_sel_hi:[1,1,0]
	v_pk_fma_f32 v[160:161], v[160:161], v[168:169], 0.5 op_sel_hi:[1,1,0]
	v_pk_fma_f32 v[162:163], v[162:163], v[170:171], 0.5 op_sel_hi:[1,1,0]
	v_pk_fma_f32 v[164:165], v[164:165], v[172:173], 0.5 op_sel_hi:[1,1,0]
	v_pk_fma_f32 v[166:167], v[166:167], v[174:175], 0.5 op_sel_hi:[1,1,0]
	v_pk_mul_f32 v[36:37], v[36:37], v[160:161]
	v_pk_mul_f32 v[38:39], v[38:39], v[162:163]
	v_pk_mul_f32 v[32:33], v[32:33], v[164:165]
	v_pk_mul_f32 v[34:35], v[34:35], v[166:167]
	v_cvt_pk_bf16_f32 v188, v36, v37
	v_cvt_pk_bf16_f32 v189, v38, v39
	v_cvt_pk_bf16_f32 v190, v32, v33
	v_cvt_pk_bf16_f32 v191, v34, v35
	global_store_dwordx4 v[196:197], v[188:191], off offset:256
	s_and_b64 vcc, exec, s[70:71]
	s_cbranch_vccz .Lg9_nostat_5
	v_pk_add_f32 v[160:161], v[44:45], v[46:47]
	v_pk_add_f32 v[162:163], v[40:41], v[42:43]
	v_pk_add_f32 v[164:165], v[36:37], v[38:39]
	v_pk_add_f32 v[166:167], v[32:33], v[34:35]
	v_pk_mul_f32 v[168:169], v[44:45], v[44:45]
	v_pk_mul_f32 v[170:171], v[36:37], v[36:37]
	v_pk_add_f32 v[160:161], v[160:161], v[162:163]
	v_pk_add_f32 v[164:165], v[164:165], v[166:167]
	v_pk_fma_f32 v[168:169], v[46:47], v[46:47], v[168:169]
	v_pk_fma_f32 v[170:171], v[38:39], v[38:39], v[170:171]
	v_pk_fma_f32 v[168:169], v[40:41], v[40:41], v[168:169]
	v_pk_fma_f32 v[170:171], v[32:33], v[32:33], v[170:171]
	v_pk_fma_f32 v[168:169], v[42:43], v[42:43], v[168:169]
	v_pk_fma_f32 v[170:171], v[34:35], v[34:35], v[170:171]
	v_pk_add_f32 v[160:161], v[160:161], v[164:165]
	v_pk_add_f32 v[168:169], v[168:169], v[170:171]
	s_nop 0
	v_add_f32_e32 v198, v160, v161
	v_add_f32_e32 v200, v168, v169
	v_mov_b32_e32 v199, v198
	s_nop 1
	v_permlane16_swap_b32 v199, v198
	s_nop 1
	v_add_f32_e32 v198, v199, v198
	v_mov_b32_e32 v202, v198
	v_mov_b32_e32 v201, v200
	s_nop 1
	v_permlane32_swap_b32 v202, v198
	s_nop 1
	s_nop 1
	v_permlane16_swap_b32 v201, v200
	s_nop 1
	v_add_f32_e32 v199, v201, v200
	v_mov_b32_e32 v203, v199
	s_nop 1
	v_permlane32_swap_b32 v203, v199
	s_nop 1
	s_and_saveexec_b64 s[4:5], s[6:7]
	v_lshlrev_b64 v[194:195], 8, v[192:193]
	v_lshl_add_u64 v[194:195], s[16:17], 0, v[194:195]
	v_lshl_add_u64 v[194:195], s[68:69], 3, v[194:195]
	v_pk_add_f32 v[200:201], v[202:203], v[198:199]
	global_store_dwordx2 v[194:195], v[200:201], off
	s_or_b64 exec, exec, s[4:5]
.Lg9_nostat_5:
	v_add_u32_e32 v192, 0xa0, v148
	v_ashrrev_i32_e32 v193, 31, v192
	v_lshlrev_b64 v[194:195], 12, v[192:193]
	v_lshl_add_u64 v[196:197], v[146:147], 0, v[194:195]
	v_pk_add_f32 v[28:29], v[28:29], v[204:205]
	v_pk_add_f32 v[30:31], v[30:31], v[206:207]
	v_pk_add_f32 v[24:25], v[24:25], v[208:209]
	v_pk_add_f32 v[26:27], v[26:27], v[210:211]
	v_med3_f32 v160, v28, s78, v158
	v_med3_f32 v161, v29, s78, v158
	v_med3_f32 v162, v30, s78, v158
	v_med3_f32 v163, v31, s78, v158
	v_med3_f32 v164, v24, s78, v158
	v_med3_f32 v165, v25, s78, v158
	v_med3_f32 v166, v26, s78, v158
	v_med3_f32 v167, v27, s78, v158
	v_pk_mul_f32 v[168:169], v[160:161], v[160:161]
	v_pk_mul_f32 v[170:171], v[162:163], v[162:163]
	v_pk_mul_f32 v[172:173], v[164:165], v[164:165]
	v_pk_mul_f32 v[174:175], v[166:167], v[166:167]
	v_pk_fma_f32 v[168:169], v[168:169], s[20:21], -1.0 op_sel_hi:[1,0,0]
	v_pk_fma_f32 v[170:171], v[170:171], s[20:21], -1.0 op_sel_hi:[1,0,0]
	v_pk_fma_f32 v[172:173], v[172:173], s[20:21], -1.0 op_sel_hi:[1,0,0]
	v_pk_fma_f32 v[174:175], v[174:175], s[20:21], -1.0 op_sel_hi:[1,0,0]
	v_pk_fma_f32 v[176:177], v[168:169], s[22:23], v[150:151] op_sel_hi:[1,0,0] neg_lo:[1,0,0] neg_hi:[1,0,0]
	v_pk_fma_f32 v[178:179], v[170:171], s[22:23], v[150:151] op_sel_hi:[1,0,0] neg_lo:[1,0,0] neg_hi:[1,0,0]
	v_pk_fma_f32 v[180:181], v[172:173], s[22:23], v[150:151] op_sel_hi:[1,0,0] neg_lo:[1,0,0] neg_hi:[1,0,0]
	v_pk_fma_f32 v[182:183], v[174:175], s[22:23], v[150:151] op_sel_hi:[1,0,0] neg_lo:[1,0,0] neg_hi:[1,0,0]
	v_pk_fma_f32 v[176:177], v[168:169], v[176:177], s[26:27] op_sel_hi:[1,1,0]
	v_pk_fma_f32 v[178:179], v[170:171], v[178:179], s[26:27] op_sel_hi:[1,1,0]
	v_pk_fma_f32 v[180:181], v[172:173], v[180:181], s[26:27] op_sel_hi:[1,1,0]
	v_pk_fma_f32 v[182:183], v[174:175], v[182:183], s[26:27] op_sel_hi:[1,1,0]
	v_pk_fma_f32 v[176:177], v[168:169], v[176:177], s[28:29] op_sel_hi:[1,1,0]
	v_pk_fma_f32 v[178:179], v[170:171], v[178:179], s[28:29] op_sel_hi:[1,1,0]
	v_pk_fma_f32 v[180:181], v[172:173], v[180:181], s[28:29] op_sel_hi:[1,1,0]
	v_pk_fma_f32 v[182:183], v[174:175], v[182:183], s[28:29] op_sel_hi:[1,1,0]
	v_pk_fma_f32 v[176:177], v[168:169], v[176:177], s[30:31] op_sel_hi:[1,1,0]
	v_pk_fma_f32 v[178:179], v[170:171], v[178:179], s[30:31] op_sel_hi:[1,1,0]
	v_pk_fma_f32 v[180:181], v[172:173], v[180:181], s[30:31] op_sel_hi:[1,1,0]
	v_pk_fma_f32 v[182:183], v[174:175], v[182:183], s[30:31] op_sel_hi:[1,1,0]
	v_pk_fma_f32 v[176:177], v[168:169], v[176:177], s[34:35] op_sel_hi:[1,1,0]
	v_pk_fma_f32 v[178:179], v[170:171], v[178:179], s[34:35] op_sel_hi:[1,1,0]
	v_pk_fma_f32 v[180:181], v[172:173], v[180:181], s[34:35] op_sel_hi:[1,1,0]
	v_pk_fma_f32 v[182:183], v[174:175], v[182:183], s[34:35] op_sel_hi:[1,1,0]
	v_pk_fma_f32 v[176:177], v[168:169], v[176:177], s[36:37] op_sel_hi:[1,1,0]
	v_pk_fma_f32 v[178:179], v[170:171], v[178:179], s[36:37] op_sel_hi:[1,1,0]
	v_pk_fma_f32 v[180:181], v[172:173], v[180:181], s[36:37] op_sel_hi:[1,1,0]
	v_pk_fma_f32 v[182:183], v[174:175], v[182:183], s[36:37] op_sel_hi:[1,1,0]
	v_pk_fma_f32 v[176:177], v[168:169], v[176:177], s[38:39] op_sel_hi:[1,1,0]
	v_pk_fma_f32 v[178:179], v[170:171], v[178:179], s[38:39] op_sel_hi:[1,1,0]
	v_pk_fma_f32 v[180:181], v[172:173], v[180:181], s[38:39] op_sel_hi:[1,1,0]
	v_pk_fma_f32 v[182:183], v[174:175], v[182:183], s[38:39] op_sel_hi:[1,1,0]
	v_pk_fma_f32 v[176:177], v[168:169], v[176:177], s[40:41] op_sel_hi:[1,1,0]
	v_pk_fma_f32 v[178:179], v[170:171], v[178:179], s[40:41] op_sel_hi:[1,1,0]
	v_pk_fma_f32 v[180:181], v[172:173], v[180:181], s[40:41] op_sel_hi:[1,1,0]
	v_pk_fma_f32 v[182:183], v[174:175], v[182:183], s[40:41] op_sel_hi:[1,1,0]
	v_pk_fma_f32 v[176:177], v[168:169], v[176:177], s[42:43] op_sel_hi:[1,1,0]
	v_pk_fma_f32 v[178:179], v[170:171], v[178:179], s[42:43] op_sel_hi:[1,1,0]
	v_pk_fma_f32 v[180:181], v[172:173], v[180:181], s[42:43] op_sel_hi:[1,1,0]
	v_pk_fma_f32 v[182:183], v[174:175], v[182:183], s[42:43] op_sel_hi:[1,1,0]
	v_pk_fma_f32 v[176:177], v[168:169], v[176:177], s[44:45] op_sel_hi:[1,1,0]
	v_pk_fma_f32 v[178:179], v[170:171], v[178:179], s[44:45] op_sel_hi:[1,1,0]
	v_pk_fma_f32 v[180:181], v[172:173], v[180:181], s[44:45] op_sel_hi:[1,1,0]
	v_pk_fma_f32 v[182:183], v[174:175], v[182:183], s[44:45] op_sel_hi:[1,1,0]
	v_pk_fma_f32 v[168:169], v[168:169], v[176:177], s[48:49] op_sel_hi:[1,1,0]
	v_pk_fma_f32 v[170:171], v[170:171], v[178:179], s[48:49] op_sel_hi:[1,1,0]
	v_pk_fma_f32 v[172:173], v[172:173], v[180:181], s[48:49] op_sel_hi:[1,1,0]
	v_pk_fma_f32 v[174:175], v[174:175], v[182:183], s[48:49] op_sel_hi:[1,1,0]
	v_pk_fma_f32 v[160:161], v[160:161], v[168:169], 0.5 op_sel_hi:[1,1,0]
	v_pk_fma_f32 v[162:163], v[162:163], v[170:171], 0.5 op_sel_hi:[1,1,0]
	v_pk_fma_f32 v[164:165], v[164:165], v[172:173], 0.5 op_sel_hi:[1,1,0]
	v_pk_fma_f32 v[166:167], v[166:167], v[174:175], 0.5 op_sel_hi:[1,1,0]
	v_pk_mul_f32 v[28:29], v[28:29], v[160:161]
	v_pk_mul_f32 v[30:31], v[30:31], v[162:163]
	v_pk_mul_f32 v[24:25], v[24:25], v[164:165]
	v_pk_mul_f32 v[26:27], v[26:27], v[166:167]
	v_cvt_pk_bf16_f32 v184, v28, v29
	v_cvt_pk_bf16_f32 v185, v30, v31
	v_cvt_pk_bf16_f32 v186, v24, v25
	v_cvt_pk_bf16_f32 v187, v26, v27
	global_store_dwordx4 v[196:197], v[184:187], off
	v_pk_add_f32 v[20:21], v[20:21], v[212:213]
	v_pk_add_f32 v[22:23], v[22:23], v[214:215]
	v_pk_add_f32 v[16:17], v[16:17], v[216:217]
	v_pk_add_f32 v[18:19], v[18:19], v[218:219]
	v_med3_f32 v160, v20, s78, v158
	v_med3_f32 v161, v21, s78, v158
	v_med3_f32 v162, v22, s78, v158
	v_med3_f32 v163, v23, s78, v158
	v_med3_f32 v164, v16, s78, v158
	v_med3_f32 v165, v17, s78, v158
	v_med3_f32 v166, v18, s78, v158
	v_med3_f32 v167, v19, s78, v158
	v_pk_mul_f32 v[168:169], v[160:161], v[160:161]
	v_pk_mul_f32 v[170:171], v[162:163], v[162:163]
	v_pk_mul_f32 v[172:173], v[164:165], v[164:165]
	v_pk_mul_f32 v[174:175], v[166:167], v[166:167]
	v_pk_fma_f32 v[168:169], v[168:169], s[20:21], -1.0 op_sel_hi:[1,0,0]
	v_pk_fma_f32 v[170:171], v[170:171], s[20:21], -1.0 op_sel_hi:[1,0,0]
	v_pk_fma_f32 v[172:173], v[172:173], s[20:21], -1.0 op_sel_hi:[1,0,0]
	v_pk_fma_f32 v[174:175], v[174:175], s[20:21], -1.0 op_sel_hi:[1,0,0]
	v_pk_fma_f32 v[176:177], v[168:169], s[22:23], v[150:151] op_sel_hi:[1,0,0] neg_lo:[1,0,0] neg_hi:[1,0,0]
	v_pk_fma_f32 v[178:179], v[170:171], s[22:23], v[150:151] op_sel_hi:[1,0,0] neg_lo:[1,0,0] neg_hi:[1,0,0]
	v_pk_fma_f32 v[180:181], v[172:173], s[22:23], v[150:151] op_sel_hi:[1,0,0] neg_lo:[1,0,0] neg_hi:[1,0,0]
	v_pk_fma_f32 v[182:183], v[174:175], s[22:23], v[150:151] op_sel_hi:[1,0,0] neg_lo:[1,0,0] neg_hi:[1,0,0]
	v_pk_fma_f32 v[176:177], v[168:169], v[176:177], s[26:27] op_sel_hi:[1,1,0]
	v_pk_fma_f32 v[178:179], v[170:171], v[178:179], s[26:27] op_sel_hi:[1,1,0]
	v_pk_fma_f32 v[180:181], v[172:173], v[180:181], s[26:27] op_sel_hi:[1,1,0]
	v_pk_fma_f32 v[182:183], v[174:175], v[182:183], s[26:27] op_sel_hi:[1,1,0]
	v_pk_fma_f32 v[176:177], v[168:169], v[176:177], s[28:29] op_sel_hi:[1,1,0]
	v_pk_fma_f32 v[178:179], v[170:171], v[178:179], s[28:29] op_sel_hi:[1,1,0]
	v_pk_fma_f32 v[180:181], v[172:173], v[180:181], s[28:29] op_sel_hi:[1,1,0]
	v_pk_fma_f32 v[182:183], v[174:175], v[182:183], s[28:29] op_sel_hi:[1,1,0]
	v_pk_fma_f32 v[176:177], v[168:169], v[176:177], s[30:31] op_sel_hi:[1,1,0]
	v_pk_fma_f32 v[178:179], v[170:171], v[178:179], s[30:31] op_sel_hi:[1,1,0]
	v_pk_fma_f32 v[180:181], v[172:173], v[180:181], s[30:31] op_sel_hi:[1,1,0]
	v_pk_fma_f32 v[182:183], v[174:175], v[182:183], s[30:31] op_sel_hi:[1,1,0]
	v_pk_fma_f32 v[176:177], v[168:169], v[176:177], s[34:35] op_sel_hi:[1,1,0]
	v_pk_fma_f32 v[178:179], v[170:171], v[178:179], s[34:35] op_sel_hi:[1,1,0]
	v_pk_fma_f32 v[180:181], v[172:173], v[180:181], s[34:35] op_sel_hi:[1,1,0]
	v_pk_fma_f32 v[182:183], v[174:175], v[182:183], s[34:35] op_sel_hi:[1,1,0]
	v_pk_fma_f32 v[176:177], v[168:169], v[176:177], s[36:37] op_sel_hi:[1,1,0]
	v_pk_fma_f32 v[178:179], v[170:171], v[178:179], s[36:37] op_sel_hi:[1,1,0]
	v_pk_fma_f32 v[180:181], v[172:173], v[180:181], s[36:37] op_sel_hi:[1,1,0]
	v_pk_fma_f32 v[182:183], v[174:175], v[182:183], s[36:37] op_sel_hi:[1,1,0]
	v_pk_fma_f32 v[176:177], v[168:169], v[176:177], s[38:39] op_sel_hi:[1,1,0]
	v_pk_fma_f32 v[178:179], v[170:171], v[178:179], s[38:39] op_sel_hi:[1,1,0]
	v_pk_fma_f32 v[180:181], v[172:173], v[180:181], s[38:39] op_sel_hi:[1,1,0]
	v_pk_fma_f32 v[182:183], v[174:175], v[182:183], s[38:39] op_sel_hi:[1,1,0]
	v_pk_fma_f32 v[176:177], v[168:169], v[176:177], s[40:41] op_sel_hi:[1,1,0]
	v_pk_fma_f32 v[178:179], v[170:171], v[178:179], s[40:41] op_sel_hi:[1,1,0]
	v_pk_fma_f32 v[180:181], v[172:173], v[180:181], s[40:41] op_sel_hi:[1,1,0]
	v_pk_fma_f32 v[182:183], v[174:175], v[182:183], s[40:41] op_sel_hi:[1,1,0]
	v_pk_fma_f32 v[176:177], v[168:169], v[176:177], s[42:43] op_sel_hi:[1,1,0]
	v_pk_fma_f32 v[178:179], v[170:171], v[178:179], s[42:43] op_sel_hi:[1,1,0]
	v_pk_fma_f32 v[180:181], v[172:173], v[180:181], s[42:43] op_sel_hi:[1,1,0]
	v_pk_fma_f32 v[182:183], v[174:175], v[182:183], s[42:43] op_sel_hi:[1,1,0]
	v_pk_fma_f32 v[176:177], v[168:169], v[176:177], s[44:45] op_sel_hi:[1,1,0]
	v_pk_fma_f32 v[178:179], v[170:171], v[178:179], s[44:45] op_sel_hi:[1,1,0]
	v_pk_fma_f32 v[180:181], v[172:173], v[180:181], s[44:45] op_sel_hi:[1,1,0]
	v_pk_fma_f32 v[182:183], v[174:175], v[182:183], s[44:45] op_sel_hi:[1,1,0]
	v_pk_fma_f32 v[168:169], v[168:169], v[176:177], s[48:49] op_sel_hi:[1,1,0]
	v_pk_fma_f32 v[170:171], v[170:171], v[178:179], s[48:49] op_sel_hi:[1,1,0]
	v_pk_fma_f32 v[172:173], v[172:173], v[180:181], s[48:49] op_sel_hi:[1,1,0]
	v_pk_fma_f32 v[174:175], v[174:175], v[182:183], s[48:49] op_sel_hi:[1,1,0]
	v_pk_fma_f32 v[160:161], v[160:161], v[168:169], 0.5 op_sel_hi:[1,1,0]
	v_pk_fma_f32 v[162:163], v[162:163], v[170:171], 0.5 op_sel_hi:[1,1,0]
	v_pk_fma_f32 v[164:165], v[164:165], v[172:173], 0.5 op_sel_hi:[1,1,0]
	v_pk_fma_f32 v[166:167], v[166:167], v[174:175], 0.5 op_sel_hi:[1,1,0]
	v_pk_mul_f32 v[20:21], v[20:21], v[160:161]
	v_pk_mul_f32 v[22:23], v[22:23], v[162:163]
	v_pk_mul_f32 v[16:17], v[16:17], v[164:165]
	v_pk_mul_f32 v[18:19], v[18:19], v[166:167]
	v_cvt_pk_bf16_f32 v188, v20, v21
	v_cvt_pk_bf16_f32 v189, v22, v23
	v_cvt_pk_bf16_f32 v190, v16, v17
	v_cvt_pk_bf16_f32 v191, v18, v19
	global_store_dwordx4 v[196:197], v[188:191], off offset:256
	s_and_b64 vcc, exec, s[70:71]
	s_cbranch_vccz .Lg9_nostat_6
	v_pk_add_f32 v[160:161], v[28:29], v[30:31]
	v_pk_add_f32 v[162:163], v[24:25], v[26:27]
	v_pk_add_f32 v[164:165], v[20:21], v[22:23]
	v_pk_add_f32 v[166:167], v[16:17], v[18:19]
	v_pk_mul_f32 v[168:169], v[28:29], v[28:29]
	v_pk_mul_f32 v[170:171], v[20:21], v[20:21]
	v_pk_add_f32 v[160:161], v[160:161], v[162:163]
	v_pk_add_f32 v[164:165], v[164:165], v[166:167]
	v_pk_fma_f32 v[168:169], v[30:31], v[30:31], v[168:169]
	v_pk_fma_f32 v[170:171], v[22:23], v[22:23], v[170:171]
	v_pk_fma_f32 v[168:169], v[24:25], v[24:25], v[168:169]
	v_pk_fma_f32 v[170:171], v[16:17], v[16:17], v[170:171]
	v_pk_fma_f32 v[168:169], v[26:27], v[26:27], v[168:169]
	v_pk_fma_f32 v[170:171], v[18:19], v[18:19], v[170:171]
	v_pk_add_f32 v[160:161], v[160:161], v[164:165]
	v_pk_add_f32 v[168:169], v[168:169], v[170:171]
	s_nop 0
	v_add_f32_e32 v198, v160, v161
	v_add_f32_e32 v200, v168, v169
	v_mov_b32_e32 v199, v198
	s_nop 1
	v_permlane16_swap_b32 v199, v198
	s_nop 1
	v_add_f32_e32 v198, v199, v198
	v_mov_b32_e32 v202, v198
	v_mov_b32_e32 v201, v200
	s_nop 1
	v_permlane32_swap_b32 v202, v198
	s_nop 1
	s_nop 1
	v_permlane16_swap_b32 v201, v200
	s_nop 1
	v_add_f32_e32 v199, v201, v200
	v_mov_b32_e32 v203, v199
	s_nop 1
	v_permlane32_swap_b32 v203, v199
	s_nop 1
	s_and_saveexec_b64 s[4:5], s[6:7]
	v_lshlrev_b64 v[194:195], 8, v[192:193]
	v_lshl_add_u64 v[194:195], s[16:17], 0, v[194:195]
	v_lshl_add_u64 v[194:195], s[68:69], 3, v[194:195]
	v_pk_add_f32 v[200:201], v[202:203], v[198:199]
	global_store_dwordx2 v[194:195], v[200:201], off
	s_or_b64 exec, exec, s[4:5]
.Lg9_nostat_6:
	v_add_u32_e32 v192, 0xb0, v148
	v_ashrrev_i32_e32 v193, 31, v192
	v_lshlrev_b64 v[194:195], 12, v[192:193]
	v_lshl_add_u64 v[196:197], v[146:147], 0, v[194:195]
	v_pk_add_f32 v[12:13], v[12:13], v[204:205]
	v_pk_add_f32 v[14:15], v[14:15], v[206:207]
	v_pk_add_f32 v[8:9], v[8:9], v[208:209]
	v_pk_add_f32 v[10:11], v[10:11], v[210:211]
	v_med3_f32 v160, v12, s78, v158
	v_med3_f32 v161, v13, s78, v158
	v_med3_f32 v162, v14, s78, v158
	v_med3_f32 v163, v15, s78, v158
	v_med3_f32 v164, v8, s78, v158
	v_med3_f32 v165, v9, s78, v158
	v_med3_f32 v166, v10, s78, v158
	v_med3_f32 v167, v11, s78, v158
	v_pk_mul_f32 v[168:169], v[160:161], v[160:161]
	v_pk_mul_f32 v[170:171], v[162:163], v[162:163]
	v_pk_mul_f32 v[172:173], v[164:165], v[164:165]
	v_pk_mul_f32 v[174:175], v[166:167], v[166:167]
	v_pk_fma_f32 v[168:169], v[168:169], s[20:21], -1.0 op_sel_hi:[1,0,0]
	v_pk_fma_f32 v[170:171], v[170:171], s[20:21], -1.0 op_sel_hi:[1,0,0]
	v_pk_fma_f32 v[172:173], v[172:173], s[20:21], -1.0 op_sel_hi:[1,0,0]
	v_pk_fma_f32 v[174:175], v[174:175], s[20:21], -1.0 op_sel_hi:[1,0,0]
	v_pk_fma_f32 v[176:177], v[168:169], s[22:23], v[150:151] op_sel_hi:[1,0,0] neg_lo:[1,0,0] neg_hi:[1,0,0]
	v_pk_fma_f32 v[178:179], v[170:171], s[22:23], v[150:151] op_sel_hi:[1,0,0] neg_lo:[1,0,0] neg_hi:[1,0,0]
	v_pk_fma_f32 v[180:181], v[172:173], s[22:23], v[150:151] op_sel_hi:[1,0,0] neg_lo:[1,0,0] neg_hi:[1,0,0]
	v_pk_fma_f32 v[182:183], v[174:175], s[22:23], v[150:151] op_sel_hi:[1,0,0] neg_lo:[1,0,0] neg_hi:[1,0,0]
	v_pk_fma_f32 v[176:177], v[168:169], v[176:177], s[26:27] op_sel_hi:[1,1,0]
	v_pk_fma_f32 v[178:179], v[170:171], v[178:179], s[26:27] op_sel_hi:[1,1,0]
	v_pk_fma_f32 v[180:181], v[172:173], v[180:181], s[26:27] op_sel_hi:[1,1,0]
	v_pk_fma_f32 v[182:183], v[174:175], v[182:183], s[26:27] op_sel_hi:[1,1,0]
	v_pk_fma_f32 v[176:177], v[168:169], v[176:177], s[28:29] op_sel_hi:[1,1,0]
	v_pk_fma_f32 v[178:179], v[170:171], v[178:179], s[28:29] op_sel_hi:[1,1,0]
	v_pk_fma_f32 v[180:181], v[172:173], v[180:181], s[28:29] op_sel_hi:[1,1,0]
	v_pk_fma_f32 v[182:183], v[174:175], v[182:183], s[28:29] op_sel_hi:[1,1,0]
	v_pk_fma_f32 v[176:177], v[168:169], v[176:177], s[30:31] op_sel_hi:[1,1,0]
	v_pk_fma_f32 v[178:179], v[170:171], v[178:179], s[30:31] op_sel_hi:[1,1,0]
	v_pk_fma_f32 v[180:181], v[172:173], v[180:181], s[30:31] op_sel_hi:[1,1,0]
	v_pk_fma_f32 v[182:183], v[174:175], v[182:183], s[30:31] op_sel_hi:[1,1,0]
	v_pk_fma_f32 v[176:177], v[168:169], v[176:177], s[34:35] op_sel_hi:[1,1,0]
	v_pk_fma_f32 v[178:179], v[170:171], v[178:179], s[34:35] op_sel_hi:[1,1,0]
	v_pk_fma_f32 v[180:181], v[172:173], v[180:181], s[34:35] op_sel_hi:[1,1,0]
	v_pk_fma_f32 v[182:183], v[174:175], v[182:183], s[34:35] op_sel_hi:[1,1,0]
	v_pk_fma_f32 v[176:177], v[168:169], v[176:177], s[36:37] op_sel_hi:[1,1,0]
	v_pk_fma_f32 v[178:179], v[170:171], v[178:179], s[36:37] op_sel_hi:[1,1,0]
	v_pk_fma_f32 v[180:181], v[172:173], v[180:181], s[36:37] op_sel_hi:[1,1,0]
	v_pk_fma_f32 v[182:183], v[174:175], v[182:183], s[36:37] op_sel_hi:[1,1,0]
	v_pk_fma_f32 v[176:177], v[168:169], v[176:177], s[38:39] op_sel_hi:[1,1,0]
	v_pk_fma_f32 v[178:179], v[170:171], v[178:179], s[38:39] op_sel_hi:[1,1,0]
	v_pk_fma_f32 v[180:181], v[172:173], v[180:181], s[38:39] op_sel_hi:[1,1,0]
	v_pk_fma_f32 v[182:183], v[174:175], v[182:183], s[38:39] op_sel_hi:[1,1,0]
	v_pk_fma_f32 v[176:177], v[168:169], v[176:177], s[40:41] op_sel_hi:[1,1,0]
	v_pk_fma_f32 v[178:179], v[170:171], v[178:179], s[40:41] op_sel_hi:[1,1,0]
	v_pk_fma_f32 v[180:181], v[172:173], v[180:181], s[40:41] op_sel_hi:[1,1,0]
	v_pk_fma_f32 v[182:183], v[174:175], v[182:183], s[40:41] op_sel_hi:[1,1,0]
	v_pk_fma_f32 v[176:177], v[168:169], v[176:177], s[42:43] op_sel_hi:[1,1,0]
	v_pk_fma_f32 v[178:179], v[170:171], v[178:179], s[42:43] op_sel_hi:[1,1,0]
	v_pk_fma_f32 v[180:181], v[172:173], v[180:181], s[42:43] op_sel_hi:[1,1,0]
	v_pk_fma_f32 v[182:183], v[174:175], v[182:183], s[42:43] op_sel_hi:[1,1,0]
	v_pk_fma_f32 v[176:177], v[168:169], v[176:177], s[44:45] op_sel_hi:[1,1,0]
	v_pk_fma_f32 v[178:179], v[170:171], v[178:179], s[44:45] op_sel_hi:[1,1,0]
	v_pk_fma_f32 v[180:181], v[172:173], v[180:181], s[44:45] op_sel_hi:[1,1,0]
	v_pk_fma_f32 v[182:183], v[174:175], v[182:183], s[44:45] op_sel_hi:[1,1,0]
	v_pk_fma_f32 v[168:169], v[168:169], v[176:177], s[48:49] op_sel_hi:[1,1,0]
	v_pk_fma_f32 v[170:171], v[170:171], v[178:179], s[48:49] op_sel_hi:[1,1,0]
	v_pk_fma_f32 v[172:173], v[172:173], v[180:181], s[48:49] op_sel_hi:[1,1,0]
	v_pk_fma_f32 v[174:175], v[174:175], v[182:183], s[48:49] op_sel_hi:[1,1,0]
	v_pk_fma_f32 v[160:161], v[160:161], v[168:169], 0.5 op_sel_hi:[1,1,0]
	v_pk_fma_f32 v[162:163], v[162:163], v[170:171], 0.5 op_sel_hi:[1,1,0]
	v_pk_fma_f32 v[164:165], v[164:165], v[172:173], 0.5 op_sel_hi:[1,1,0]
	v_pk_fma_f32 v[166:167], v[166:167], v[174:175], 0.5 op_sel_hi:[1,1,0]
	v_pk_mul_f32 v[12:13], v[12:13], v[160:161]
	v_pk_mul_f32 v[14:15], v[14:15], v[162:163]
	v_pk_mul_f32 v[8:9], v[8:9], v[164:165]
	v_pk_mul_f32 v[10:11], v[10:11], v[166:167]
	v_cvt_pk_bf16_f32 v184, v12, v13
	v_cvt_pk_bf16_f32 v185, v14, v15
	v_cvt_pk_bf16_f32 v186, v8, v9
	v_cvt_pk_bf16_f32 v187, v10, v11
	global_store_dwordx4 v[196:197], v[184:187], off
	v_pk_add_f32 v[4:5], v[4:5], v[212:213]
	v_pk_add_f32 v[6:7], v[6:7], v[214:215]
	v_pk_add_f32 v[0:1], v[0:1], v[216:217]
	v_pk_add_f32 v[2:3], v[2:3], v[218:219]
	v_med3_f32 v160, v4, s78, v158
	v_med3_f32 v161, v5, s78, v158
	v_med3_f32 v162, v6, s78, v158
	v_med3_f32 v163, v7, s78, v158
	v_med3_f32 v164, v0, s78, v158
	v_med3_f32 v165, v1, s78, v158
	v_med3_f32 v166, v2, s78, v158
	v_med3_f32 v167, v3, s78, v158
	v_pk_mul_f32 v[168:169], v[160:161], v[160:161]
	v_pk_mul_f32 v[170:171], v[162:163], v[162:163]
	v_pk_mul_f32 v[172:173], v[164:165], v[164:165]
	v_pk_mul_f32 v[174:175], v[166:167], v[166:167]
	v_pk_fma_f32 v[168:169], v[168:169], s[20:21], -1.0 op_sel_hi:[1,0,0]
	v_pk_fma_f32 v[170:171], v[170:171], s[20:21], -1.0 op_sel_hi:[1,0,0]
	v_pk_fma_f32 v[172:173], v[172:173], s[20:21], -1.0 op_sel_hi:[1,0,0]
	v_pk_fma_f32 v[174:175], v[174:175], s[20:21], -1.0 op_sel_hi:[1,0,0]
	v_pk_fma_f32 v[176:177], v[168:169], s[22:23], v[150:151] op_sel_hi:[1,0,0] neg_lo:[1,0,0] neg_hi:[1,0,0]
	v_pk_fma_f32 v[178:179], v[170:171], s[22:23], v[150:151] op_sel_hi:[1,0,0] neg_lo:[1,0,0] neg_hi:[1,0,0]
	v_pk_fma_f32 v[180:181], v[172:173], s[22:23], v[150:151] op_sel_hi:[1,0,0] neg_lo:[1,0,0] neg_hi:[1,0,0]
	v_pk_fma_f32 v[182:183], v[174:175], s[22:23], v[150:151] op_sel_hi:[1,0,0] neg_lo:[1,0,0] neg_hi:[1,0,0]
	v_pk_fma_f32 v[176:177], v[168:169], v[176:177], s[26:27] op_sel_hi:[1,1,0]
	v_pk_fma_f32 v[178:179], v[170:171], v[178:179], s[26:27] op_sel_hi:[1,1,0]
	v_pk_fma_f32 v[180:181], v[172:173], v[180:181], s[26:27] op_sel_hi:[1,1,0]
	v_pk_fma_f32 v[182:183], v[174:175], v[182:183], s[26:27] op_sel_hi:[1,1,0]
	v_pk_fma_f32 v[176:177], v[168:169], v[176:177], s[28:29] op_sel_hi:[1,1,0]
	v_pk_fma_f32 v[178:179], v[170:171], v[178:179], s[28:29] op_sel_hi:[1,1,0]
	v_pk_fma_f32 v[180:181], v[172:173], v[180:181], s[28:29] op_sel_hi:[1,1,0]
	v_pk_fma_f32 v[182:183], v[174:175], v[182:183], s[28:29] op_sel_hi:[1,1,0]
	v_pk_fma_f32 v[176:177], v[168:169], v[176:177], s[30:31] op_sel_hi:[1,1,0]
	v_pk_fma_f32 v[178:179], v[170:171], v[178:179], s[30:31] op_sel_hi:[1,1,0]
	v_pk_fma_f32 v[180:181], v[172:173], v[180:181], s[30:31] op_sel_hi:[1,1,0]
	v_pk_fma_f32 v[182:183], v[174:175], v[182:183], s[30:31] op_sel_hi:[1,1,0]
	v_pk_fma_f32 v[176:177], v[168:169], v[176:177], s[34:35] op_sel_hi:[1,1,0]
	v_pk_fma_f32 v[178:179], v[170:171], v[178:179], s[34:35] op_sel_hi:[1,1,0]
	v_pk_fma_f32 v[180:181], v[172:173], v[180:181], s[34:35] op_sel_hi:[1,1,0]
	v_pk_fma_f32 v[182:183], v[174:175], v[182:183], s[34:35] op_sel_hi:[1,1,0]
	v_pk_fma_f32 v[176:177], v[168:169], v[176:177], s[36:37] op_sel_hi:[1,1,0]
	v_pk_fma_f32 v[178:179], v[170:171], v[178:179], s[36:37] op_sel_hi:[1,1,0]
	v_pk_fma_f32 v[180:181], v[172:173], v[180:181], s[36:37] op_sel_hi:[1,1,0]
	v_pk_fma_f32 v[182:183], v[174:175], v[182:183], s[36:37] op_sel_hi:[1,1,0]
	v_pk_fma_f32 v[176:177], v[168:169], v[176:177], s[38:39] op_sel_hi:[1,1,0]
	v_pk_fma_f32 v[178:179], v[170:171], v[178:179], s[38:39] op_sel_hi:[1,1,0]
	v_pk_fma_f32 v[180:181], v[172:173], v[180:181], s[38:39] op_sel_hi:[1,1,0]
	v_pk_fma_f32 v[182:183], v[174:175], v[182:183], s[38:39] op_sel_hi:[1,1,0]
	v_pk_fma_f32 v[176:177], v[168:169], v[176:177], s[40:41] op_sel_hi:[1,1,0]
	v_pk_fma_f32 v[178:179], v[170:171], v[178:179], s[40:41] op_sel_hi:[1,1,0]
	v_pk_fma_f32 v[180:181], v[172:173], v[180:181], s[40:41] op_sel_hi:[1,1,0]
	v_pk_fma_f32 v[182:183], v[174:175], v[182:183], s[40:41] op_sel_hi:[1,1,0]
	v_pk_fma_f32 v[176:177], v[168:169], v[176:177], s[42:43] op_sel_hi:[1,1,0]
	v_pk_fma_f32 v[178:179], v[170:171], v[178:179], s[42:43] op_sel_hi:[1,1,0]
	v_pk_fma_f32 v[180:181], v[172:173], v[180:181], s[42:43] op_sel_hi:[1,1,0]
	v_pk_fma_f32 v[182:183], v[174:175], v[182:183], s[42:43] op_sel_hi:[1,1,0]
	v_pk_fma_f32 v[176:177], v[168:169], v[176:177], s[44:45] op_sel_hi:[1,1,0]
	v_pk_fma_f32 v[178:179], v[170:171], v[178:179], s[44:45] op_sel_hi:[1,1,0]
	v_pk_fma_f32 v[180:181], v[172:173], v[180:181], s[44:45] op_sel_hi:[1,1,0]
	v_pk_fma_f32 v[182:183], v[174:175], v[182:183], s[44:45] op_sel_hi:[1,1,0]
	v_pk_fma_f32 v[168:169], v[168:169], v[176:177], s[48:49] op_sel_hi:[1,1,0]
	v_pk_fma_f32 v[170:171], v[170:171], v[178:179], s[48:49] op_sel_hi:[1,1,0]
	v_pk_fma_f32 v[172:173], v[172:173], v[180:181], s[48:49] op_sel_hi:[1,1,0]
	v_pk_fma_f32 v[174:175], v[174:175], v[182:183], s[48:49] op_sel_hi:[1,1,0]
	v_pk_fma_f32 v[160:161], v[160:161], v[168:169], 0.5 op_sel_hi:[1,1,0]
	v_pk_fma_f32 v[162:163], v[162:163], v[170:171], 0.5 op_sel_hi:[1,1,0]
	v_pk_fma_f32 v[164:165], v[164:165], v[172:173], 0.5 op_sel_hi:[1,1,0]
	v_pk_fma_f32 v[166:167], v[166:167], v[174:175], 0.5 op_sel_hi:[1,1,0]
	v_pk_mul_f32 v[4:5], v[4:5], v[160:161]
	v_pk_mul_f32 v[6:7], v[6:7], v[162:163]
	v_pk_mul_f32 v[0:1], v[0:1], v[164:165]
	v_pk_mul_f32 v[2:3], v[2:3], v[166:167]
	v_cvt_pk_bf16_f32 v188, v4, v5
	v_cvt_pk_bf16_f32 v189, v6, v7
	v_cvt_pk_bf16_f32 v190, v0, v1
	v_cvt_pk_bf16_f32 v191, v2, v3
	global_store_dwordx4 v[196:197], v[188:191], off offset:256
	s_and_b64 vcc, exec, s[70:71]
	s_cbranch_vccz .Lg9_nostat_7
	v_pk_add_f32 v[160:161], v[12:13], v[14:15]
	v_pk_add_f32 v[162:163], v[8:9], v[10:11]
	v_pk_add_f32 v[164:165], v[4:5], v[6:7]
	v_pk_add_f32 v[166:167], v[0:1], v[2:3]
	v_pk_mul_f32 v[168:169], v[12:13], v[12:13]
	v_pk_mul_f32 v[170:171], v[4:5], v[4:5]
	v_pk_add_f32 v[160:161], v[160:161], v[162:163]
	v_pk_add_f32 v[164:165], v[164:165], v[166:167]
	v_pk_fma_f32 v[168:169], v[14:15], v[14:15], v[168:169]
	v_pk_fma_f32 v[170:171], v[6:7], v[6:7], v[170:171]
	v_pk_fma_f32 v[168:169], v[8:9], v[8:9], v[168:169]
	v_pk_fma_f32 v[170:171], v[0:1], v[0:1], v[170:171]
	v_pk_fma_f32 v[168:169], v[10:11], v[10:11], v[168:169]
	v_pk_fma_f32 v[170:171], v[2:3], v[2:3], v[170:171]
	v_pk_add_f32 v[160:161], v[160:161], v[164:165]
	v_pk_add_f32 v[168:169], v[168:169], v[170:171]
	s_nop 0
	v_add_f32_e32 v198, v160, v161
	v_add_f32_e32 v200, v168, v169
	v_mov_b32_e32 v199, v198
	s_nop 1
	v_permlane16_swap_b32 v199, v198
	s_nop 1
	v_add_f32_e32 v198, v199, v198
	v_mov_b32_e32 v202, v198
	v_mov_b32_e32 v201, v200
	s_nop 1
	v_permlane32_swap_b32 v202, v198
	s_nop 1
	s_nop 1
	v_permlane16_swap_b32 v201, v200
	s_nop 1
	v_add_f32_e32 v199, v201, v200
	v_mov_b32_e32 v203, v199
	s_nop 1
	v_permlane32_swap_b32 v203, v199
	s_nop 1
	s_and_saveexec_b64 s[4:5], s[6:7]
	v_lshlrev_b64 v[194:195], 8, v[192:193]
	v_lshl_add_u64 v[194:195], s[16:17], 0, v[194:195]
	v_lshl_add_u64 v[194:195], s[68:69], 3, v[194:195]
	v_pk_add_f32 v[200:201], v[202:203], v[198:199]
	global_store_dwordx2 v[194:195], v[200:201], off
	s_or_b64 exec, exec, s[4:5]

	.amdhsa_kernel _Z4mega5MArgs
		.amdhsa_group_segment_fixed_size 0
		.amdhsa_private_segment_fixed_size 0
		.amdhsa_kernarg_size 496
		.amdhsa_user_sgpr_count 2
		.amdhsa_user_sgpr_dispatch_ptr 0
		.amdhsa_user_sgpr_queue_ptr 0
		.amdhsa_user_sgpr_kernarg_segment_ptr 1
		.amdhsa_user_sgpr_dispatch_id 0
		.amdhsa_user_sgpr_kernarg_preload_length 0
		.amdhsa_user_sgpr_kernarg_preload_offset 0
		.amdhsa_user_sgpr_private_segment_size 0
		.amdhsa_uses_dynamic_stack 0
		.amdhsa_enable_private_segment 0
		.amdhsa_system_sgpr_workgroup_id_x 1
		.amdhsa_system_sgpr_workgroup_id_y 0
		.amdhsa_system_sgpr_workgroup_id_z 0
		.amdhsa_system_sgpr_workgroup_info 0
		.amdhsa_system_vgpr_workitem_id 0
		.amdhsa_next_free_vgpr 250
		.amdhsa_next_free_sgpr 102
		.amdhsa_accum_offset 252
		.amdhsa_reserve_vcc 1
		.amdhsa_float_round_mode_32 0
		.amdhsa_float_round_mode_16_64 0
		.amdhsa_float_denorm_mode_32 3
		.amdhsa_float_denorm_mode_16_64 3
		.amdhsa_dx10_clamp 1
		.amdhsa_ieee_mode 1
		.amdhsa_fp16_overflow 0
		.amdhsa_tg_split 0
		.amdhsa_exception_fp_ieee_invalid_op 0
		.amdhsa_exception_fp_denorm_src 0
		.amdhsa_exception_fp_ieee_div_zero 0
		.amdhsa_exception_fp_ieee_overflow 0
		.amdhsa_exception_fp_ieee_underflow 0
		.amdhsa_exception_fp_ieee_inexact 0
		.amdhsa_exception_int_div_zero 0
	.end_amdhsa_kernel

amdhsa.kernels:
  - .agpr_count:     0
    .args:
      - .offset:         0
        .size:           240
        .value_kind:     by_value
      - .offset:         240
        .size:           4
        .value_kind:     hidden_block_count_x
      - .offset:         244
        .size:           4
        .value_kind:     hidden_block_count_y
      - .offset:         248
        .size:           4
        .value_kind:     hidden_block_count_z
      - .offset:         252
        .size:           2
        .value_kind:     hidden_group_size_x
      - .offset:         254
        .size:           2
        .value_kind:     hidden_group_size_y
      - .offset:         256
        .size:           2
        .value_kind:     hidden_group_size_z
      - .offset:         258
        .size:           2
        .value_kind:     hidden_remainder_x
      - .offset:         260
        .size:           2
        .value_kind:     hidden_remainder_y
      - .offset:         262
        .size:           2
        .value_kind:     hidden_remainder_z
      - .offset:         280
        .size:           8
        .value_kind:     hidden_global_offset_x
      - .offset:         288
        .size:           8
        .value_kind:     hidden_global_offset_y
      - .offset:         296
        .size:           8
        .value_kind:     hidden_global_offset_z
      - .offset:         304
        .size:           2
        .value_kind:     hidden_grid_dims
      - .offset:         360
        .size:           4
        .value_kind:     hidden_dynamic_lds_size
    .group_segment_fixed_size: 0
    .kernarg_segment_align: 8
    .kernarg_segment_size: 496
    .language:       OpenCL C
    .language_version:
      - 2
      - 0
    .max_flat_workgroup_size: 512
    .name:           _Z4mega5MArgs
    .private_segment_fixed_size: 0
    .sgpr_count:     108
    .sgpr_spill_count: 65
    .symbol:         _Z4mega5MArgs.kd
    .uniform_work_group_size: 1
    .uses_dynamic_stack: false
    .vgpr_count:     250
    .vgpr_spill_count: 0
    .wavefront_size: 64
